# topk stage-1 keys: index subtract + constant add fused into one add (per-lane constants pre-biased inside the token loop); softmax row maxima via v_max_f32_dpp
# baseline (speedup 1.0000x reference)
.LBB0_1844:
	v_readlane_b32 s0, v253, 60
	v_readlane_b32 s1, v253, 61
	s_andn2_b64 vcc, exec, s[0:1]
	s_cbranch_vccnz .LBB0_1876
	v_and_b32_e32 v33, -8, v32
	v_cmp_eq_u32_e64 s[44:45], 16, v33
	v_subrev_u32_e32 v46, 24, v32
	v_subrev_u32_e32 v47, 29, v32
	v_cndmask_b32_e64 v51, 0, 4, s[44:45]
	v_cmp_lt_u32_e64 s[44:45], 4, v46
	v_subrev_u32_e32 v48, 33, v32
	v_and_b32_e32 v49, -2, v32
	v_cndmask_b32_e64 v46, 8, v51, s[44:45]
	v_cmp_lt_u32_e64 s[44:45], 3, v47
	v_cmp_eq_u32_e32 vcc, 1, v32
	s_mov_b32 s0, s38
	v_cndmask_b32_e64 v46, 12, v46, s[44:45]
	v_cmp_lt_u32_e64 s[44:45], 2, v48
	v_writelane_b32 v255, s0, 45
	v_readlane_b32 s8, v251, 38
	v_cndmask_b32_e64 v46, 16, v46, s[44:45]
	v_cmp_ne_u32_e64 s[44:45], 36, v49
	v_writelane_b32 v255, s1, 46
	v_lshlrev_b32_e32 v44, 4, v32
	v_cndmask_b32_e64 v46, 20, v46, s[44:45]
	v_cmp_ne_u32_e64 s[44:45], 38, v49
	v_readlane_b32 s9, v251, 39
	v_lshlrev_b32_e32 v36, 5, v32
	v_cndmask_b32_e64 v46, 24, v46, s[44:45]
	v_cmp_ne_u32_e64 s[44:45], 40, v49
	v_lshlrev_b32_e32 v38, 3, v32
	v_add_u32_e32 v42, 0x400, v44
	v_cndmask_b32_e64 v46, 28, v46, s[44:45]
	v_cmp_ne_u32_e64 s[44:45], 42, v32
	v_readlane_b32 s8, v255, 4
	v_ashrrev_i32_e32 v37, 31, v36
	v_cndmask_b32_e64 v46, 32, v46, s[44:45]
	v_cmp_ne_u32_e64 s[44:45], 43, v32
	v_and_b32_e32 v139, 0x78, v38
	v_and_b32_e32 v100, 0xffffff80, v38
	v_cndmask_b32_e64 v46, 36, v46, s[44:45]
	v_cmp_ne_u32_e64 s[44:45], 44, v32
	v_ashrrev_i32_e32 v38, 3, v32
	v_ashrrev_i32_e32 v42, 7, v42
	v_cndmask_b32_e64 v46, 40, v46, s[44:45]
	v_cmp_ne_u32_e64 s[44:45], 45, v32
	v_readlane_b32 s9, v255, 5
	s_lshl_b32 s4, s38, 11
	v_cndmask_b32_e64 v46, 44, v46, s[44:45]
	v_cmp_ne_u32_e64 s[44:45], 46, v32
	v_ashrrev_i32_e32 v39, 31, v38
	v_ashrrev_i32_e32 v43, 31, v42
	v_cndmask_b32_e64 v46, 48, v46, s[44:45]
	v_cmp_ne_u32_e64 s[44:45], 47, v32
	v_lshl_add_u64 v[122:123], s[8:9], 0, v[36:37]
	v_readlane_b32 s8, v255, 10
	v_cndmask_b32_e64 v46, 52, v46, s[44:45]
	v_cmp_ne_u32_e64 s[44:45], 48, v32
	s_cmp_lg_u32 s38, 3
	v_lshlrev_b64 v[40:41], 21, v[38:39]
	v_cndmask_b32_e64 v46, 56, v46, s[44:45]
	v_cmp_ne_u32_e64 s[44:45], 49, v32
	v_lshlrev_b64 v[42:43], 21, v[42:43]
	v_readlane_b32 s9, v255, 11
	v_cndmask_b32_e64 v146, 60, v46, s[44:45]
	v_cndmask_b32_e64 v46, 0, 4, vcc
	v_cmp_ne_u32_e32 vcc, 2, v32
	s_cselect_b64 s[68:69], -1, 0
	s_add_i32 s94, s4, 0x800
	v_cndmask_b32_e32 v46, 8, v46, vcc
	v_cmp_ne_u32_e32 vcc, 3, v32
	v_lshl_add_u64 v[124:125], s[8:9], 0, v[42:43]
	v_lshl_add_u64 v[126:127], s[8:9], 0, v[40:41]
	v_cndmask_b32_e32 v46, 12, v46, vcc
	v_cmp_ne_u32_e32 vcc, 4, v32
	v_readlane_b32 s8, v255, 18
	s_mov_b64 s[62:63], s[52:53]
	v_cndmask_b32_e32 v46, 16, v46, vcc
	v_cmp_ne_u32_e32 vcc, 5, v32
	s_lshl_b64 s[52:53], s[94:95], 2
	v_readlane_b32 s20, v251, 50
	v_cndmask_b32_e32 v46, 20, v46, vcc
	v_cmp_ne_u32_e32 vcc, 6, v32
	v_readlane_b32 s9, v255, 19
	v_subrev_u32_e32 v50, 42, v32
	v_cndmask_b32_e32 v46, 24, v46, vcc
	v_cmp_ne_u32_e32 vcc, 7, v32
	v_ashrrev_i32_e32 v33, 31, v32
	v_ashrrev_i32_e32 v45, 31, v44
	v_cndmask_b32_e32 v46, 28, v46, vcc
	v_cmp_ne_u32_e32 vcc, 8, v32
	v_readlane_b32 s21, v251, 51
	s_add_u32 s52, s20, s52
	v_cndmask_b32_e32 v46, 32, v46, vcc
	v_cmp_ne_u32_e32 vcc, 9, v32
	v_lshl_add_u64 v[128:129], s[8:9], 0, v[42:43]
	v_lshl_add_u64 v[130:131], s[8:9], 0, v[40:41]
	v_cndmask_b32_e32 v46, 36, v46, vcc
	v_cmp_ne_u32_e32 vcc, 10, v32
	v_readlane_b32 s8, v255, 24
	v_lshlrev_b64 v[34:35], 2, v[32:33]
	v_cndmask_b32_e32 v46, 40, v46, vcc
	v_cmp_ne_u32_e32 vcc, 11, v32
	v_ashrrev_i32_e32 v33, 4, v32
	s_addc_u32 s53, s21, s53
	v_cndmask_b32_e32 v46, 44, v46, vcc
	v_cmp_ne_u32_e32 vcc, 12, v32
	v_lshlrev_b64 v[110:111], 2, v[44:45]
	v_readlane_b32 s9, v255, 25
	v_cndmask_b32_e32 v46, 48, v46, vcc
	v_cmp_ne_u32_e32 vcc, 13, v32
	v_cmp_gt_u32_e64 s[4:5], 50, v32
	v_cmp_eq_u32_e64 s[78:79], 0, v32
	v_cndmask_b32_e32 v46, 52, v46, vcc
	v_cmp_ne_u32_e32 vcc, 14, v32
	v_cmp_gt_i32_e64 s[76:77], 32, v32
	v_and_b32_e32 v140, 15, v32
	v_cndmask_b32_e32 v46, 56, v46, vcc
	v_cmp_ne_u32_e32 vcc, 15, v32
	v_sub_u32_e32 v141, 63, v32
	v_lshl_add_u32 v142, v32, 2, s84
	v_cndmask_b32_e32 v46, 60, v46, vcc
	v_cmp_ne_u32_e32 vcc, 16, v32
	v_cmp_gt_u32_e64 s[44:45], 16, v32
	v_cmp_eq_u32_e64 s[46:47], 1, v33
	v_cndmask_b32_e32 v46, 0, v46, vcc
	v_cmp_ne_u32_e32 vcc, 17, v32
	v_cmp_eq_u32_e64 s[48:49], 2, v33
	v_cmp_eq_u32_e64 s[50:51], 3, v33
	v_cndmask_b32_e32 v46, 4, v46, vcc
	v_cmp_ne_u32_e32 vcc, 18, v32
	v_add_u32_e32 v33, 64, v32
	v_lshl_add_u64 v[112:113], s[52:53], 0, v[110:111]
	v_cndmask_b32_e32 v46, 8, v46, vcc
	v_cmp_ne_u32_e32 vcc, 19, v32
	s_mov_b64 s[52:53], 0x1010
	v_lshl_add_u64 v[132:133], s[8:9], 0, v[34:35]
	v_cndmask_b32_e32 v46, 12, v46, vcc
	v_cmp_ne_u32_e32 vcc, 20, v32
	v_readlane_b32 s8, v255, 26
	v_readlane_b32 s18, v251, 48
	v_cndmask_b32_e32 v46, 16, v46, vcc
	v_cmp_ne_u32_e32 vcc, 21, v32
	v_readlane_b32 s19, v251, 49
	v_readlane_b32 s22, v251, 52
	v_cndmask_b32_e32 v46, 20, v46, vcc
	v_cmp_ne_u32_e32 vcc, 22, v32
	v_readlane_b32 s23, v251, 53
	v_lshl_add_u64 v[116:117], v[112:113], 0, s[52:53]
	v_cndmask_b32_e32 v46, 24, v46, vcc
	v_cmp_ne_u32_e32 vcc, 23, v32
	s_mov_b64 s[52:53], 0x1020
	v_readlane_b32 s9, v255, 27
	v_cndmask_b32_e32 v46, 28, v46, vcc
	v_cmp_ne_u32_e32 vcc, 24, v32
	v_lshlrev_b32_e32 v200, 1, v139
	v_add_u32_e32 v104, 0x200, v100
	v_cndmask_b32_e32 v46, 0, v46, vcc
	v_cmp_ne_u32_e32 vcc, 25, v32
	v_add_u32_e32 v106, 0x400, v100
	v_add_u32_e32 v108, 0x600, v100
	v_cndmask_b32_e32 v46, 4, v46, vcc
	v_cmp_ne_u32_e32 vcc, 26, v32
	v_readlane_b32 s12, v251, 42
	v_readlane_b32 s13, v251, 43
	v_cndmask_b32_e32 v46, 8, v46, vcc
	v_cmp_ne_u32_e32 vcc, 27, v32
	v_readlane_b32 s14, v251, 44
	v_readlane_b32 s15, v251, 45
	v_cndmask_b32_e32 v46, 12, v46, vcc
	v_cmp_ne_u32_e32 vcc, 28, v32
	s_mov_b64 s[22:23], s[76:77]
	s_mov_b64 s[18:19], s[68:69]
	v_cndmask_b32_e32 v46, 16, v46, vcc
	v_cmp_ne_u32_e32 vcc, 29, v32
	v_lshl_add_u64 v[118:119], v[112:113], 0, s[52:53]
	s_mov_b64 s[52:53], 0x1030
	v_cndmask_b32_e32 v46, 0, v46, vcc
	v_cmp_ne_u32_e32 vcc, 30, v32
	v_readlane_b32 s68, v255, 16
	v_readlane_b32 s76, v254, 62
	v_cndmask_b32_e32 v46, 4, v46, vcc
	v_cmp_ne_u32_e32 vcc, 31, v32
	s_waitcnt vmcnt(0)
	v_lshl_add_u64 v[96:97], s[66:67], 0, v[34:35]
	v_lshl_add_u64 v[98:99], v[36:37], 1, s[70:71]
	v_cndmask_b32_e32 v46, 8, v46, vcc
	v_cmp_ne_u32_e32 vcc, 32, v32
	v_lshl_add_u64 v[102:103], s[96:97], 0, v[200:201]
	v_and_b32_e32 v200, 0x70, v44
	v_cndmask_b32_e32 v46, 12, v46, vcc
	v_cmp_ne_u32_e32 vcc, 33, v32
	v_or_b32_e32 v143, 1, v139
	v_or_b32_e32 v144, 2, v139
	v_cndmask_b32_e32 v46, 0, v46, vcc
	v_cmp_ne_u32_e32 vcc, 34, v32
	v_or_b32_e32 v145, 3, v139
	v_ashrrev_i32_e32 v101, 31, v100
	v_cndmask_b32_e32 v46, 4, v46, vcc
	v_cmp_ne_u32_e32 vcc, 35, v32
	v_ashrrev_i32_e32 v105, 31, v104
	v_ashrrev_i32_e32 v107, 31, v106
	v_cndmask_b32_e32 v46, 8, v46, vcc
	v_cmp_ne_u32_e32 vcc, 36, v32
	v_ashrrev_i32_e32 v109, 31, v108
	v_cmp_eq_u32_e64 s[0:1], 0, v140
	v_cndmask_b32_e32 v46, 0, v46, vcc
	v_cmp_ne_u32_e32 vcc, 37, v32
	v_cmp_eq_u32_e64 s[54:55], 1, v140
	v_cmp_eq_u32_e64 s[64:65], 2, v140
	v_cndmask_b32_e32 v46, 4, v46, vcc
	v_cmp_ne_u32_e32 vcc, 38, v32
	v_cmp_eq_u32_e64 s[2:3], 3, v140
	v_cmp_eq_u32_e64 s[6:7], 4, v140
	v_cndmask_b32_e32 v46, 0, v46, vcc
	v_cmp_ne_u32_e32 vcc, 39, v32
	v_cmp_eq_u32_e64 s[96:97], 5, v140
	v_cmp_eq_u32_e64 s[66:67], 6, v140
	v_cndmask_b32_e32 v46, 4, v46, vcc
	v_cmp_ne_u32_e32 vcc, 40, v32
	v_cmp_eq_u32_e64 s[24:25], 7, v140
	v_cmp_eq_u32_e64 s[26:27], 8, v140
	v_cndmask_b32_e32 v46, 0, v46, vcc
	v_cmp_ne_u32_e32 vcc, 41, v32
	v_and_b32_e32 v32, 7, v32
	v_lshlrev_b32_e32 v32, 6, v32
	v_cndmask_b32_e32 v46, 4, v46, vcc
	v_cmp_lt_u32_e32 vcc, 7, v50
	v_cmp_eq_u32_e64 s[28:29], 9, v140
	v_cmp_eq_u32_e64 s[30:31], 10, v140
	v_cndmask_b32_e32 v46, 0, v46, vcc
	v_add_u32_e32 v147, 64, v46
	v_add_u32_e32 v149, 0xc0, v46
	v_ashrrev_i32_e32 v46, 3, v33
	v_mov_b32_e32 v33, v201
	v_ashrrev_i32_e32 v47, 31, v46
	v_lshl_add_u64 v[32:33], s[8:9], 0, v[32:33]
	v_cmp_eq_u32_e64 s[34:35], 11, v140
	v_cmp_eq_u32_e64 s[36:37], 12, v140
	v_cmp_eq_u32_e64 s[38:39], 13, v140
	v_cmp_eq_u32_e64 s[40:41], 14, v140
	v_cmp_eq_u32_e64 s[42:43], 15, v140
	v_add_u32_e32 v148, 0x80, v146
	v_or_b32_e32 v150, 16, v140
	v_or_b32_e32 v151, 32, v140
	v_or_b32_e32 v152, 48, v140
	s_mov_b64 s[20:21], s[78:79]
	v_lshl_add_u64 v[114:115], v[112:113], 0, s[60:61]
	v_lshl_add_u64 v[120:121], v[112:113], 0, s[52:53]
	v_lshl_add_u64 v[134:135], v[38:39], 2, v[32:33]
	v_lshl_add_u64 v[136:137], v[46:47], 2, v[32:33]
	v_readlane_b32 s69, v255, 17
	s_mov_b64 s[14:15], s[62:63]
	s_mov_b64 s[12:13], s[74:75]
	v_readlane_b32 s77, v254, 63
	s_mov_b32 s8, s80
	v_readlane_b32 s10, v251, 40
	v_readlane_b32 s11, v251, 41
	v_readlane_b32 s16, v251, 46
	v_readlane_b32 s17, v251, 47
	v_mov_b32_e32 v226, 0x30c0400
	v_mov_b32_e32 v228, 0x3040100
	v_mov_b32_e32 v242, 0x4b400000
	v_sub_u32_e32 v139, 0x7f, v139
	v_sub_u32_e32 v143, 0x7f, v143
	v_sub_u32_e32 v144, 0x7f, v144
	v_sub_u32_e32 v145, 0x7f, v145
	s_branch .LBB0_1848

.LBB0_1852:
	s_or_b64 exec, exec, s[80:81]
	v_lshlrev_b32_e32 v16, 16, v12
	v_and_b32_e32 v17, 0xffff0000, v12
	v_bfe_i32 v24, v12, 15, 1
	s_mov_b32 s9, 0x7fffff80
	v_ashrrev_i32_e32 v12, 31, v12
	v_lshlrev_b32_e32 v18, 16, v13
	v_bitop3_b32 v12, v12, v17, s9 bitop3:0x6c
	v_bfe_i32 v17, v13, 15, 1
	v_and_b32_e32 v19, 0xffff0000, v13
	v_lshlrev_b32_e32 v20, 16, v14
	v_and_b32_e32 v21, 0xffff0000, v14
	v_lshlrev_b32_e32 v22, 16, v15
	v_and_b32_e32 v23, 0xffff0000, v15
	v_bitop3_b32 v16, v24, v16, s9 bitop3:0x6c
	v_bfe_i32 v24, v14, 15, 1
	v_ashrrev_i32_e32 v14, 31, v14
	v_bitop3_b32 v17, v17, v18, s9 bitop3:0x6c
	v_bfe_i32 v18, v15, 15, 1
	v_ashrrev_i32_e32 v13, 31, v13
	v_ashrrev_i32_e32 v15, 31, v15
	v_bitop3_b32 v20, v24, v20, s9 bitop3:0x6c
	v_bitop3_b32 v14, v14, v21, s9 bitop3:0x6c
	v_bitop3_b32 v18, v18, v22, s9 bitop3:0x6c
	v_bitop3_b32 v13, v13, v19, s9 bitop3:0x6c
	v_bitop3_b32 v15, v15, v23, s9 bitop3:0x6c
	v_add_u32_e32 v16, v16, v139
	v_add3_u32 v20, v20, v139, -4
	v_add_u32_e32 v12, v12, v143
	v_add3_u32 v14, v14, v143, -4
	v_add_u32_e32 v17, v17, v144
	v_add3_u32 v18, v18, v144, -4
	v_add_u32_e32 v13, v13, v145
	v_add3_u32 v15, v15, v145, -4
	v_max_i32_e32 v19, v16, v12
	v_min_i32_e32 v12, v16, v12
	v_max_i32_e32 v16, v17, v13
	v_min_i32_e32 v13, v17, v13
	v_max_i32_e32 v17, v20, v14
	v_min_i32_e32 v14, v20, v14
	v_max_i32_e32 v20, v18, v15
	v_min_i32_e32 v15, v18, v15
	v_max_i32_e32 v18, v19, v16
	v_min_i32_e32 v16, v19, v16
	v_max_i32_e32 v19, v12, v13
	v_min_i32_e32 v12, v12, v13
	v_max_i32_e32 v13, v17, v20
	v_min_i32_e32 v17, v17, v20
	v_max_i32_e32 v20, v14, v15
	v_min_i32_e32 v14, v14, v15
	v_max_i32_e32 v15, v19, v16
	v_min_i32_e32 v16, v19, v16
	v_max_i32_e32 v19, v20, v17
	v_min_i32_e32 v17, v20, v17
	v_max_i32_e32 v154, v18, v13
	v_min_i32_e32 v13, v18, v13
	v_max_i32_e32 v18, v15, v19
	v_min_i32_e32 v15, v15, v19
	v_max_i32_e32 v19, v16, v17
	v_min_i32_e32 v16, v16, v17
	v_max_i32_e32 v17, v12, v14
	v_min_i32_e32 v155, v12, v14
	v_max_i32_e32 v12, v19, v13
	v_min_i32_e32 v13, v19, v13
	v_max_i32_e32 v14, v17, v15
	v_max_i32_e32 v156, v18, v12
	v_min_i32_e32 v157, v18, v12
	v_max_i32_e32 v158, v14, v13
	v_min_i32_e32 v159, v14, v13
	v_lshlrev_b32_e32 v12, 16, v8
	v_and_b32_e32 v13, 0xffff0000, v8
	v_bfe_i32 v20, v8, 15, 1
	v_ashrrev_i32_e32 v8, 31, v8
	v_min_i32_e32 v15, v17, v15
	v_lshlrev_b32_e32 v14, 16, v9
	v_bitop3_b32 v8, v8, v13, s9 bitop3:0x6c
	v_bfe_i32 v13, v9, 15, 1
	v_max_i32_e32 v160, v15, v16
	v_min_i32_e32 v161, v15, v16
	v_and_b32_e32 v15, 0xffff0000, v9
	v_lshlrev_b32_e32 v16, 16, v10
	v_and_b32_e32 v17, 0xffff0000, v10
	v_lshlrev_b32_e32 v18, 16, v11
	v_and_b32_e32 v19, 0xffff0000, v11
	v_bitop3_b32 v12, v20, v12, s9 bitop3:0x6c
	v_bfe_i32 v20, v10, 15, 1
	v_ashrrev_i32_e32 v10, 31, v10
	v_bitop3_b32 v13, v13, v14, s9 bitop3:0x6c
	v_bfe_i32 v14, v11, 15, 1
	v_ashrrev_i32_e32 v9, 31, v9
	v_ashrrev_i32_e32 v11, 31, v11
	v_bitop3_b32 v16, v20, v16, s9 bitop3:0x6c
	v_bitop3_b32 v10, v10, v17, s9 bitop3:0x6c
	v_bitop3_b32 v14, v14, v18, s9 bitop3:0x6c
	v_bitop3_b32 v9, v9, v15, s9 bitop3:0x6c
	v_bitop3_b32 v11, v11, v19, s9 bitop3:0x6c
	v_add_u32_e32 v12, v12, v139
	v_add3_u32 v16, v16, v139, -4
	v_add_u32_e32 v8, v8, v143
	v_add3_u32 v10, v10, v143, -4
	v_add_u32_e32 v13, v13, v144
	v_add3_u32 v14, v14, v144, -4
	v_add_u32_e32 v9, v9, v145
	v_add3_u32 v11, v11, v145, -4
	v_max_i32_e32 v15, v12, v8
	v_min_i32_e32 v8, v12, v8
	v_max_i32_e32 v12, v13, v9
	v_min_i32_e32 v9, v13, v9
	v_max_i32_e32 v13, v16, v10
	v_min_i32_e32 v10, v16, v10
	v_max_i32_e32 v16, v14, v11
	v_min_i32_e32 v11, v14, v11
	v_max_i32_e32 v14, v15, v12
	v_min_i32_e32 v12, v15, v12
	v_max_i32_e32 v15, v8, v9
	v_min_i32_e32 v8, v8, v9
	v_max_i32_e32 v9, v13, v16
	v_min_i32_e32 v13, v13, v16
	v_max_i32_e32 v16, v10, v11
	v_min_i32_e32 v10, v10, v11
	v_max_i32_e32 v11, v15, v12
	v_min_i32_e32 v12, v15, v12
	v_max_i32_e32 v15, v16, v13
	v_min_i32_e32 v13, v16, v13
	v_max_i32_e32 v162, v14, v9
	v_min_i32_e32 v9, v14, v9
	v_max_i32_e32 v14, v11, v15
	v_min_i32_e32 v11, v11, v15
	v_max_i32_e32 v15, v12, v13
	v_min_i32_e32 v12, v12, v13
	v_max_i32_e32 v13, v8, v10
	v_min_i32_e32 v163, v8, v10
	v_max_i32_e32 v8, v15, v9
	v_min_i32_e32 v9, v15, v9
	v_max_i32_e32 v10, v13, v11
	v_max_i32_e32 v164, v14, v8
	v_min_i32_e32 v165, v14, v8
	v_max_i32_e32 v166, v10, v9
	v_min_i32_e32 v167, v10, v9
	v_lshlrev_b32_e32 v8, 16, v4
	v_and_b32_e32 v9, 0xffff0000, v4
	v_bfe_i32 v16, v4, 15, 1
	v_ashrrev_i32_e32 v4, 31, v4
	v_min_i32_e32 v11, v13, v11
	v_lshlrev_b32_e32 v10, 16, v5
	v_bitop3_b32 v4, v4, v9, s9 bitop3:0x6c
	v_bfe_i32 v9, v5, 15, 1
	v_max_i32_e32 v168, v11, v12
	v_min_i32_e32 v169, v11, v12
	v_and_b32_e32 v11, 0xffff0000, v5
	v_lshlrev_b32_e32 v12, 16, v6
	v_and_b32_e32 v13, 0xffff0000, v6
	v_lshlrev_b32_e32 v14, 16, v7
	v_and_b32_e32 v15, 0xffff0000, v7
	v_bitop3_b32 v8, v16, v8, s9 bitop3:0x6c
	v_bfe_i32 v16, v6, 15, 1
	v_ashrrev_i32_e32 v6, 31, v6
	v_bitop3_b32 v9, v9, v10, s9 bitop3:0x6c
	v_bfe_i32 v10, v7, 15, 1
	v_ashrrev_i32_e32 v5, 31, v5
	v_ashrrev_i32_e32 v7, 31, v7
	v_bitop3_b32 v12, v16, v12, s9 bitop3:0x6c
	v_bitop3_b32 v6, v6, v13, s9 bitop3:0x6c
	v_bitop3_b32 v10, v10, v14, s9 bitop3:0x6c
	v_bitop3_b32 v5, v5, v11, s9 bitop3:0x6c
	v_bitop3_b32 v7, v7, v15, s9 bitop3:0x6c
	v_add_u32_e32 v8, v8, v139
	v_add3_u32 v12, v12, v139, -4
	v_add_u32_e32 v4, v4, v143
	v_add3_u32 v6, v6, v143, -4
	v_add_u32_e32 v9, v9, v144
	v_add3_u32 v10, v10, v144, -4
	v_add_u32_e32 v5, v5, v145
	v_add3_u32 v7, v7, v145, -4
	v_max_i32_e32 v11, v8, v4
	v_min_i32_e32 v4, v8, v4
	v_max_i32_e32 v8, v9, v5
	v_min_i32_e32 v5, v9, v5
	v_max_i32_e32 v9, v12, v6
	v_min_i32_e32 v6, v12, v6
	v_max_i32_e32 v12, v10, v7
	v_min_i32_e32 v7, v10, v7
	v_max_i32_e32 v10, v11, v8
	v_min_i32_e32 v8, v11, v8
	v_max_i32_e32 v11, v4, v5
	v_min_i32_e32 v4, v4, v5
	v_max_i32_e32 v5, v9, v12
	v_min_i32_e32 v9, v9, v12
	v_max_i32_e32 v12, v6, v7
	v_min_i32_e32 v6, v6, v7
	v_max_i32_e32 v7, v11, v8
	v_min_i32_e32 v8, v11, v8
	v_max_i32_e32 v11, v12, v9
	v_min_i32_e32 v9, v12, v9
	v_max_i32_e32 v170, v10, v5
	v_min_i32_e32 v5, v10, v5
	v_max_i32_e32 v10, v7, v11
	v_min_i32_e32 v7, v7, v11
	v_max_i32_e32 v11, v8, v9
	v_min_i32_e32 v8, v8, v9
	v_max_i32_e32 v9, v4, v6
	v_min_i32_e32 v171, v4, v6
	v_max_i32_e32 v4, v11, v5
	v_min_i32_e32 v5, v11, v5
	v_max_i32_e32 v6, v9, v7
	v_max_i32_e32 v172, v10, v4
	v_min_i32_e32 v173, v10, v4
	v_max_i32_e32 v174, v6, v5
	v_min_i32_e32 v175, v6, v5
	v_lshlrev_b32_e32 v4, 16, v0
	v_and_b32_e32 v5, 0xffff0000, v0
	v_bfe_i32 v12, v0, 15, 1
	v_ashrrev_i32_e32 v0, 31, v0
	v_min_i32_e32 v7, v9, v7
	v_lshlrev_b32_e32 v6, 16, v1
	v_bitop3_b32 v0, v0, v5, s9 bitop3:0x6c
	v_bfe_i32 v5, v1, 15, 1
	v_max_i32_e32 v176, v7, v8
	v_min_i32_e32 v177, v7, v8
	v_and_b32_e32 v7, 0xffff0000, v1
	v_lshlrev_b32_e32 v8, 16, v2
	v_and_b32_e32 v9, 0xffff0000, v2
	v_lshlrev_b32_e32 v10, 16, v3
	v_and_b32_e32 v11, 0xffff0000, v3
	v_bitop3_b32 v4, v12, v4, s9 bitop3:0x6c
	v_bfe_i32 v12, v2, 15, 1
	v_ashrrev_i32_e32 v2, 31, v2
	v_bitop3_b32 v5, v5, v6, s9 bitop3:0x6c
	v_bfe_i32 v6, v3, 15, 1
	v_ashrrev_i32_e32 v1, 31, v1
	v_ashrrev_i32_e32 v3, 31, v3
	v_max_i32_dpp v153, v154, v154 row_ror:1 row_mask:0xf bank_mask:0xf bound_ctrl:1
	v_bitop3_b32 v8, v12, v8, s9 bitop3:0x6c
	v_bitop3_b32 v2, v2, v9, s9 bitop3:0x6c
	v_bitop3_b32 v6, v6, v10, s9 bitop3:0x6c
	v_bitop3_b32 v1, v1, v7, s9 bitop3:0x6c
	v_bitop3_b32 v3, v3, v11, s9 bitop3:0x6c
	v_max_i32_dpp v153, v153, v153 row_ror:2 row_mask:0xf bank_mask:0xf bound_ctrl:1
	v_add_u32_e32 v4, v4, v139
	v_add3_u32 v8, v8, v139, -4
	v_add_u32_e32 v0, v0, v143
	v_add3_u32 v2, v2, v143, -4
	v_add_u32_e32 v5, v5, v144
	v_add3_u32 v6, v6, v144, -4
	v_add_u32_e32 v1, v1, v145
	v_add3_u32 v3, v3, v145, -4
	v_max_i32_dpp v153, v153, v153 row_ror:4 row_mask:0xf bank_mask:0xf bound_ctrl:1
	s_nop 1
	v_max_i32_dpp v153, v153, v153 row_ror:8 row_mask:0xf bank_mask:0xf bound_ctrl:1
	v_max_i32_e32 v7, v4, v0
	v_min_i32_e32 v0, v4, v0
	v_max_i32_e32 v4, v5, v1
	v_min_i32_e32 v1, v5, v1
	v_max_i32_e32 v5, v8, v2
	v_min_i32_e32 v2, v8, v2
	v_max_i32_e32 v8, v6, v3
	v_cmp_eq_u32_e32 vcc, v154, v153
	v_min_i32_e32 v3, v6, v3
	v_max_i32_e32 v6, v7, v4
	v_min_i32_e32 v4, v7, v4
	v_max_i32_e32 v7, v0, v1
	v_min_i32_e32 v0, v0, v1
	v_max_i32_e32 v1, v5, v8
	v_cndmask_b32_e32 v186, v154, v156, vcc
	v_max_i32_dpp v154, v162, v162 row_ror:1 row_mask:0xf bank_mask:0xf bound_ctrl:1
	v_max_i32_e32 v178, v6, v1
	v_cndmask_b32_e32 v188, v157, v158, vcc
	v_cndmask_b32_e32 v158, v158, v159, vcc
	v_cndmask_b32_e32 v159, v159, v160, vcc
	v_cndmask_b32_e32 v160, v160, v161, vcc
	v_cndmask_b32_e32 v161, v161, v155, vcc
	v_cndmask_b32_e32 v189, v155, v237, vcc
	v_max_i32_dpp v154, v154, v154 row_ror:2 row_mask:0xf bank_mask:0xf bound_ctrl:1
	v_max_i32_dpp v155, v170, v170 row_ror:1 row_mask:0xf bank_mask:0xf bound_ctrl:1
	v_min_i32_e32 v5, v5, v8
	v_max_i32_e32 v8, v2, v3
	v_cndmask_b32_e32 v187, v156, v157, vcc
	v_max_i32_dpp v154, v154, v154 row_ror:4 row_mask:0xf bank_mask:0xf bound_ctrl:1
	v_max_i32_dpp v155, v155, v155 row_ror:2 row_mask:0xf bank_mask:0xf bound_ctrl:1
	v_max_i32_dpp v156, v178, v178 row_ror:1 row_mask:0xf bank_mask:0xf bound_ctrl:1
	v_min_i32_e32 v2, v2, v3
	v_max_i32_e32 v3, v7, v4
	v_min_i32_e32 v4, v7, v4
	v_max_i32_e32 v7, v8, v5
	v_min_i32_e32 v5, v8, v5
	v_max_i32_dpp v154, v154, v154 row_ror:8 row_mask:0xf bank_mask:0xf bound_ctrl:1
	v_max_i32_dpp v155, v155, v155 row_ror:4 row_mask:0xf bank_mask:0xf bound_ctrl:1
	v_max_i32_dpp v156, v156, v156 row_ror:2 row_mask:0xf bank_mask:0xf bound_ctrl:1
	v_max_i32_dpp v157, v186, v186 row_ror:1 row_mask:0xf bank_mask:0xf bound_ctrl:1
	v_min_i32_e32 v1, v6, v1
	v_max_i32_e32 v6, v3, v7
	v_min_i32_e32 v3, v3, v7
	v_max_i32_e32 v7, v4, v5
	v_min_i32_e32 v4, v4, v5
	v_max_i32_e32 v5, v0, v2
	v_cmp_eq_u32_e32 vcc, v162, v154
	v_max_i32_dpp v155, v155, v155 row_ror:8 row_mask:0xf bank_mask:0xf bound_ctrl:1
	v_max_i32_dpp v156, v156, v156 row_ror:4 row_mask:0xf bank_mask:0xf bound_ctrl:1
	v_max_i32_dpp v157, v157, v157 row_ror:2 row_mask:0xf bank_mask:0xf bound_ctrl:1
	v_min_i32_e32 v179, v0, v2
	v_max_i32_e32 v0, v7, v1
	v_min_i32_e32 v1, v7, v1
	v_max_i32_e32 v2, v5, v3
	v_min_i32_e32 v3, v5, v3
	v_cndmask_b32_e32 v162, v162, v164, vcc
	v_cndmask_b32_e32 v164, v164, v165, vcc
	v_cndmask_b32_e32 v165, v165, v166, vcc
	v_cndmask_b32_e32 v166, v166, v167, vcc
	v_cndmask_b32_e32 v167, v167, v168, vcc
	v_cndmask_b32_e32 v168, v168, v169, vcc
	v_cndmask_b32_e32 v169, v169, v163, vcc
	v_cndmask_b32_e32 v163, v163, v237, vcc
	v_cmp_eq_u32_e32 vcc, v170, v155
	v_max_i32_dpp v156, v156, v156 row_ror:8 row_mask:0xf bank_mask:0xf bound_ctrl:1
	v_max_i32_dpp v157, v157, v157 row_ror:4 row_mask:0xf bank_mask:0xf bound_ctrl:1
	v_max_i32_e32 v180, v6, v0
	v_min_i32_e32 v181, v6, v0
	v_max_i32_e32 v182, v2, v1
	v_min_i32_e32 v183, v2, v1
	v_max_i32_e32 v184, v3, v4
	v_min_i32_e32 v185, v3, v4
	v_cndmask_b32_e32 v170, v170, v172, vcc
	v_cndmask_b32_e32 v172, v172, v173, vcc
	v_cndmask_b32_e32 v173, v173, v174, vcc
	v_cndmask_b32_e32 v174, v174, v175, vcc
	v_cndmask_b32_e32 v175, v175, v176, vcc
	v_cndmask_b32_e32 v176, v176, v177, vcc
	v_cndmask_b32_e32 v177, v177, v171, vcc
	v_cndmask_b32_e32 v171, v171, v237, vcc
	v_cmp_eq_u32_e32 vcc, v178, v156
	v_max_i32_dpp v157, v157, v157 row_ror:8 row_mask:0xf bank_mask:0xf bound_ctrl:1
	s_lshl_b64 s[52:53], s[52:53], 12
	v_cndmask_b32_e32 v178, v178, v180, vcc
	v_cndmask_b32_e32 v180, v180, v181, vcc
	v_cndmask_b32_e32 v181, v181, v182, vcc
	v_cndmask_b32_e32 v182, v182, v183, vcc
	v_cndmask_b32_e32 v183, v183, v184, vcc
	v_cndmask_b32_e32 v184, v184, v185, vcc
	v_cndmask_b32_e32 v185, v185, v179, vcc
	v_cndmask_b32_e32 v179, v179, v237, vcc
	v_cmp_eq_u32_e32 vcc, v186, v157
	v_lshl_add_u64 v[0:1], v[98:99], 0, s[52:53]
	global_load_dwordx4 v[16:19], v[0:1], off offset:48
	global_load_dwordx4 v[20:23], v[0:1], off offset:32
	global_load_dwordx4 v[24:27], v[0:1], off offset:16
	global_load_dwordx4 v[28:31], v[0:1], off
	v_cndmask_b32_e32 v186, v186, v187, vcc
	v_cndmask_b32_e32 v187, v187, v188, vcc
	v_cndmask_b32_e32 v188, v188, v158, vcc
	v_cndmask_b32_e32 v190, v158, v159, vcc
	v_max_i32_dpp v158, v162, v162 row_ror:1 row_mask:0xf bank_mask:0xf bound_ctrl:1
	v_cndmask_b32_e32 v191, v159, v160, vcc
	v_max_i32_dpp v159, v170, v170 row_ror:1 row_mask:0xf bank_mask:0xf bound_ctrl:1
	v_max_i32_dpp v158, v158, v158 row_ror:2 row_mask:0xf bank_mask:0xf bound_ctrl:1
	v_cndmask_b32_e32 v192, v160, v161, vcc
	v_cndmask_b32_e32 v193, v161, v189, vcc
	v_max_i32_dpp v158, v158, v158 row_ror:4 row_mask:0xf bank_mask:0xf bound_ctrl:1
	v_cndmask_b32_e32 v189, v189, v237, vcc
	v_max_i32_dpp v159, v159, v159 row_ror:2 row_mask:0xf bank_mask:0xf bound_ctrl:1
	v_max_i32_dpp v158, v158, v158 row_ror:8 row_mask:0xf bank_mask:0xf bound_ctrl:1
	v_cmp_eq_u32_e32 vcc, v162, v158
	v_max_i32_dpp v160, v178, v178 row_ror:1 row_mask:0xf bank_mask:0xf bound_ctrl:1
	v_max_i32_dpp v159, v159, v159 row_ror:4 row_mask:0xf bank_mask:0xf bound_ctrl:1
	v_cndmask_b32_e32 v194, v162, v164, vcc
	v_max_i32_dpp v160, v160, v160 row_ror:2 row_mask:0xf bank_mask:0xf bound_ctrl:1
	v_max_i32_dpp v161, v186, v186 row_ror:1 row_mask:0xf bank_mask:0xf bound_ctrl:1
	v_max_i32_dpp v159, v159, v159 row_ror:8 row_mask:0xf bank_mask:0xf bound_ctrl:1
	v_max_i32_dpp v160, v160, v160 row_ror:4 row_mask:0xf bank_mask:0xf bound_ctrl:1
	v_max_i32_dpp v161, v161, v161 row_ror:2 row_mask:0xf bank_mask:0xf bound_ctrl:1
	v_max_i32_dpp v162, v194, v194 row_ror:1 row_mask:0xf bank_mask:0xf bound_ctrl:1
	v_cndmask_b32_e32 v164, v164, v165, vcc
	v_cndmask_b32_e32 v165, v165, v166, vcc
	v_cndmask_b32_e32 v166, v166, v167, vcc
	v_cndmask_b32_e32 v167, v167, v168, vcc
	v_cndmask_b32_e32 v168, v168, v169, vcc
	v_cndmask_b32_e32 v169, v169, v163, vcc
	v_cndmask_b32_e32 v163, v163, v237, vcc
	v_cmp_eq_u32_e32 vcc, v170, v159
	v_max_i32_dpp v160, v160, v160 row_ror:8 row_mask:0xf bank_mask:0xf bound_ctrl:1
	v_max_i32_dpp v161, v161, v161 row_ror:4 row_mask:0xf bank_mask:0xf bound_ctrl:1
	v_max_i32_dpp v162, v162, v162 row_ror:2 row_mask:0xf bank_mask:0xf bound_ctrl:1
	v_cndmask_b32_e32 v170, v170, v172, vcc
	v_cndmask_b32_e32 v172, v172, v173, vcc
	v_cndmask_b32_e32 v173, v173, v174, vcc
	v_cndmask_b32_e32 v174, v174, v175, vcc
	v_cndmask_b32_e32 v175, v175, v176, vcc
	v_cndmask_b32_e32 v176, v176, v177, vcc
	v_cndmask_b32_e32 v177, v177, v171, vcc
	v_cndmask_b32_e32 v171, v171, v237, vcc
	v_cmp_eq_u32_e32 vcc, v178, v160
	v_max_i32_dpp v161, v161, v161 row_ror:8 row_mask:0xf bank_mask:0xf bound_ctrl:1
	v_max_i32_dpp v162, v162, v162 row_ror:4 row_mask:0xf bank_mask:0xf bound_ctrl:1
	v_cndmask_b32_e32 v178, v178, v180, vcc
	v_cndmask_b32_e32 v180, v180, v181, vcc
	v_cndmask_b32_e32 v181, v181, v182, vcc
	v_cndmask_b32_e32 v182, v182, v183, vcc
	v_cndmask_b32_e32 v183, v183, v184, vcc
	v_cndmask_b32_e32 v184, v184, v185, vcc
	v_cndmask_b32_e32 v185, v185, v179, vcc
	v_cndmask_b32_e32 v179, v179, v237, vcc
	v_cmp_eq_u32_e32 vcc, v186, v161
	v_max_i32_dpp v162, v162, v162 row_ror:8 row_mask:0xf bank_mask:0xf bound_ctrl:1
	v_lshl_add_u64 v[0:1], v[102:103], 0, s[52:53]
	v_cndmask_b32_e32 v186, v186, v187, vcc
	v_cndmask_b32_e32 v187, v187, v188, vcc
	v_cndmask_b32_e32 v188, v188, v190, vcc
	v_cndmask_b32_e32 v190, v190, v191, vcc
	v_cndmask_b32_e32 v191, v191, v192, vcc
	v_cndmask_b32_e32 v192, v192, v193, vcc
	v_cndmask_b32_e32 v193, v193, v189, vcc
	v_cndmask_b32_e32 v189, v189, v237, vcc
	v_cmp_eq_u32_e32 vcc, v194, v162
	v_lshl_add_u64 v[2:3], v[100:101], 1, v[0:1]
	v_lshl_add_u64 v[4:5], v[104:105], 1, v[0:1]
	v_cndmask_b32_e32 v197, v166, v167, vcc
	v_cndmask_b32_e32 v167, v167, v168, vcc
	v_cndmask_b32_e32 v168, v168, v169, vcc
	v_cndmask_b32_e32 v169, v169, v163, vcc
	v_cndmask_b32_e32 v198, v163, v237, vcc
	v_max_i32_dpp v163, v170, v170 row_ror:1 row_mask:0xf bank_mask:0xf bound_ctrl:1
	v_cndmask_b32_e32 v194, v194, v164, vcc
	v_cndmask_b32_e32 v195, v164, v165, vcc
	v_max_i32_dpp v163, v163, v163 row_ror:2 row_mask:0xf bank_mask:0xf bound_ctrl:1
	v_max_i32_dpp v164, v178, v178 row_ror:1 row_mask:0xf bank_mask:0xf bound_ctrl:1
	v_cndmask_b32_e32 v196, v165, v166, vcc
	v_max_i32_dpp v163, v163, v163 row_ror:4 row_mask:0xf bank_mask:0xf bound_ctrl:1
	v_max_i32_dpp v164, v164, v164 row_ror:2 row_mask:0xf bank_mask:0xf bound_ctrl:1
	v_max_i32_dpp v165, v186, v186 row_ror:1 row_mask:0xf bank_mask:0xf bound_ctrl:1
	v_max_i32_dpp v163, v163, v163 row_ror:8 row_mask:0xf bank_mask:0xf bound_ctrl:1
	v_max_i32_dpp v164, v164, v164 row_ror:4 row_mask:0xf bank_mask:0xf bound_ctrl:1
	v_max_i32_dpp v165, v165, v165 row_ror:2 row_mask:0xf bank_mask:0xf bound_ctrl:1
	v_max_i32_dpp v166, v194, v194 row_ror:1 row_mask:0xf bank_mask:0xf bound_ctrl:1
	v_cmp_eq_u32_e32 vcc, v170, v163
	v_max_i32_dpp v164, v164, v164 row_ror:8 row_mask:0xf bank_mask:0xf bound_ctrl:1
	v_max_i32_dpp v165, v165, v165 row_ror:4 row_mask:0xf bank_mask:0xf bound_ctrl:1
	v_max_i32_dpp v166, v166, v166 row_ror:2 row_mask:0xf bank_mask:0xf bound_ctrl:1
	v_cndmask_b32_e32 v170, v170, v172, vcc
	v_cndmask_b32_e32 v172, v172, v173, vcc
	v_cndmask_b32_e32 v173, v173, v174, vcc
	v_cndmask_b32_e32 v174, v174, v175, vcc
	v_cndmask_b32_e32 v175, v175, v176, vcc
	v_cndmask_b32_e32 v176, v176, v177, vcc
	v_cndmask_b32_e32 v177, v177, v171, vcc
	v_cndmask_b32_e32 v171, v171, v237, vcc
	v_cmp_eq_u32_e32 vcc, v178, v164
	v_max_i32_dpp v165, v165, v165 row_ror:8 row_mask:0xf bank_mask:0xf bound_ctrl:1
	v_max_i32_dpp v166, v166, v166 row_ror:4 row_mask:0xf bank_mask:0xf bound_ctrl:1
	v_cndmask_b32_e32 v178, v178, v180, vcc
	v_cndmask_b32_e32 v180, v180, v181, vcc
	v_cndmask_b32_e32 v181, v181, v182, vcc
	v_cndmask_b32_e32 v182, v182, v183, vcc
	v_cndmask_b32_e32 v183, v183, v184, vcc
	v_cndmask_b32_e32 v184, v184, v185, vcc
	v_cndmask_b32_e32 v185, v185, v179, vcc
	v_cndmask_b32_e32 v179, v179, v237, vcc
	v_cmp_eq_u32_e32 vcc, v186, v165
	v_max_i32_dpp v166, v166, v166 row_ror:8 row_mask:0xf bank_mask:0xf bound_ctrl:1
	global_load_dwordx4 v[12:15], v[2:3], off
	global_load_dwordx4 v[8:11], v[4:5], off
	v_cndmask_b32_e32 v186, v186, v187, vcc
	v_cndmask_b32_e32 v187, v187, v188, vcc
	v_cndmask_b32_e32 v188, v188, v190, vcc
	v_cndmask_b32_e32 v190, v190, v191, vcc
	v_cndmask_b32_e32 v191, v191, v192, vcc
	v_cndmask_b32_e32 v192, v192, v193, vcc
	v_cndmask_b32_e32 v193, v193, v189, vcc
	v_cndmask_b32_e32 v189, v189, v237, vcc
	v_cmp_eq_u32_e32 vcc, v194, v166
	v_lshl_add_u64 v[2:3], v[106:107], 1, v[0:1]
	v_lshl_add_u64 v[0:1], v[108:109], 1, v[0:1]
	v_cndmask_b32_e32 v194, v194, v195, vcc
	v_cndmask_b32_e32 v195, v195, v196, vcc
	v_cndmask_b32_e32 v196, v196, v197, vcc
	v_cndmask_b32_e32 v197, v197, v167, vcc
	v_cndmask_b32_e32 v199, v167, v168, vcc
	v_max_i32_dpp v167, v170, v170 row_ror:1 row_mask:0xf bank_mask:0xf bound_ctrl:1
	v_cndmask_b32_e32 v203, v168, v169, vcc
	v_max_i32_dpp v168, v178, v178 row_ror:1 row_mask:0xf bank_mask:0xf bound_ctrl:1
	v_max_i32_dpp v167, v167, v167 row_ror:2 row_mask:0xf bank_mask:0xf bound_ctrl:1
	v_cndmask_b32_e32 v204, v169, v198, vcc
	v_cndmask_b32_e32 v198, v198, v237, vcc
	v_max_i32_dpp v167, v167, v167 row_ror:4 row_mask:0xf bank_mask:0xf bound_ctrl:1
	v_max_i32_dpp v168, v168, v168 row_ror:2 row_mask:0xf bank_mask:0xf bound_ctrl:1
	v_max_i32_dpp v169, v186, v186 row_ror:1 row_mask:0xf bank_mask:0xf bound_ctrl:1
	v_max_i32_dpp v167, v167, v167 row_ror:8 row_mask:0xf bank_mask:0xf bound_ctrl:1
	v_cmp_eq_u32_e32 vcc, v170, v167
	v_max_i32_dpp v168, v168, v168 row_ror:4 row_mask:0xf bank_mask:0xf bound_ctrl:1
	v_max_i32_dpp v169, v169, v169 row_ror:2 row_mask:0xf bank_mask:0xf bound_ctrl:1
	v_cndmask_b32_e32 v205, v170, v172, vcc
	v_max_i32_dpp v170, v194, v194 row_ror:1 row_mask:0xf bank_mask:0xf bound_ctrl:1
	v_cndmask_b32_e32 v172, v172, v173, vcc
	v_cndmask_b32_e32 v173, v173, v174, vcc
	v_cndmask_b32_e32 v174, v174, v175, vcc
	v_cndmask_b32_e32 v175, v175, v176, vcc
	v_cndmask_b32_e32 v176, v176, v177, vcc
	v_cndmask_b32_e32 v177, v177, v171, vcc
	v_cndmask_b32_e32 v206, v171, v237, vcc
	v_max_i32_dpp v168, v168, v168 row_ror:8 row_mask:0xf bank_mask:0xf bound_ctrl:1
	v_max_i32_dpp v169, v169, v169 row_ror:4 row_mask:0xf bank_mask:0xf bound_ctrl:1
	v_max_i32_dpp v170, v170, v170 row_ror:2 row_mask:0xf bank_mask:0xf bound_ctrl:1
	v_max_i32_dpp v171, v205, v205 row_ror:1 row_mask:0xf bank_mask:0xf bound_ctrl:1
	v_cmp_eq_u32_e32 vcc, v178, v168
	v_max_i32_dpp v169, v169, v169 row_ror:8 row_mask:0xf bank_mask:0xf bound_ctrl:1
	v_max_i32_dpp v170, v170, v170 row_ror:4 row_mask:0xf bank_mask:0xf bound_ctrl:1
	v_max_i32_dpp v171, v171, v171 row_ror:2 row_mask:0xf bank_mask:0xf bound_ctrl:1
	v_cndmask_b32_e32 v178, v178, v180, vcc
	v_cndmask_b32_e32 v180, v180, v181, vcc
	v_cndmask_b32_e32 v181, v181, v182, vcc
	v_cndmask_b32_e32 v182, v182, v183, vcc
	v_cndmask_b32_e32 v183, v183, v184, vcc
	v_cndmask_b32_e32 v184, v184, v185, vcc
	v_cndmask_b32_e32 v185, v185, v179, vcc
	v_cndmask_b32_e32 v179, v179, v237, vcc
	v_cmp_eq_u32_e32 vcc, v186, v169
	v_max_i32_dpp v170, v170, v170 row_ror:8 row_mask:0xf bank_mask:0xf bound_ctrl:1
	v_max_i32_dpp v171, v171, v171 row_ror:4 row_mask:0xf bank_mask:0xf bound_ctrl:1
	v_cndmask_b32_e32 v186, v186, v187, vcc
	v_cndmask_b32_e32 v187, v187, v188, vcc
	v_cndmask_b32_e32 v188, v188, v190, vcc
	v_cndmask_b32_e32 v190, v190, v191, vcc
	v_cndmask_b32_e32 v191, v191, v192, vcc
	v_cndmask_b32_e32 v192, v192, v193, vcc
	v_cndmask_b32_e32 v193, v193, v189, vcc
	v_cndmask_b32_e32 v189, v189, v237, vcc
	v_cmp_eq_u32_e32 vcc, v194, v170
	v_max_i32_dpp v171, v171, v171 row_ror:8 row_mask:0xf bank_mask:0xf bound_ctrl:1
	global_load_dwordx4 v[4:7], v[2:3], off
	s_nop 0
	global_load_dwordx4 v[0:3], v[0:1], off
	v_cndmask_b32_e32 v194, v194, v195, vcc
	v_cndmask_b32_e32 v195, v195, v196, vcc
	v_cndmask_b32_e32 v196, v196, v197, vcc
	v_cndmask_b32_e32 v197, v197, v199, vcc
	v_cndmask_b32_e32 v199, v199, v203, vcc
	v_cndmask_b32_e32 v203, v203, v204, vcc
	v_cndmask_b32_e32 v204, v204, v198, vcc
	v_cndmask_b32_e32 v198, v198, v237, vcc
	v_cmp_eq_u32_e32 vcc, v205, v171
	v_mov_b32_e32 v241, v201
	s_nop 0
	v_cndmask_b32_e32 v205, v205, v172, vcc
	v_cndmask_b32_e32 v207, v172, v173, vcc
	v_max_i32_dpp v172, v178, v178 row_ror:1 row_mask:0xf bank_mask:0xf bound_ctrl:1
	v_cndmask_b32_e32 v208, v173, v174, vcc
	v_max_i32_dpp v173, v186, v186 row_ror:1 row_mask:0xf bank_mask:0xf bound_ctrl:1
	v_max_i32_dpp v172, v172, v172 row_ror:2 row_mask:0xf bank_mask:0xf bound_ctrl:1
	v_cndmask_b32_e32 v209, v174, v175, vcc
	v_max_i32_dpp v173, v173, v173 row_ror:2 row_mask:0xf bank_mask:0xf bound_ctrl:1
	v_max_i32_dpp v172, v172, v172 row_ror:4 row_mask:0xf bank_mask:0xf bound_ctrl:1
	v_max_i32_dpp v174, v194, v194 row_ror:1 row_mask:0xf bank_mask:0xf bound_ctrl:1
	v_cndmask_b32_e32 v210, v175, v176, vcc
	v_max_i32_dpp v172, v172, v172 row_ror:8 row_mask:0xf bank_mask:0xf bound_ctrl:1
	v_max_i32_dpp v173, v173, v173 row_ror:4 row_mask:0xf bank_mask:0xf bound_ctrl:1
	v_max_i32_dpp v174, v174, v174 row_ror:2 row_mask:0xf bank_mask:0xf bound_ctrl:1
	v_max_i32_dpp v175, v205, v205 row_ror:1 row_mask:0xf bank_mask:0xf bound_ctrl:1
	v_cndmask_b32_e32 v176, v176, v177, vcc
	v_cndmask_b32_e32 v177, v177, v206, vcc
	v_cndmask_b32_e32 v206, v206, v237, vcc
	v_cmp_eq_u32_e32 vcc, v178, v172
	v_max_i32_dpp v173, v173, v173 row_ror:8 row_mask:0xf bank_mask:0xf bound_ctrl:1
	v_max_i32_dpp v174, v174, v174 row_ror:4 row_mask:0xf bank_mask:0xf bound_ctrl:1
	v_max_i32_dpp v175, v175, v175 row_ror:2 row_mask:0xf bank_mask:0xf bound_ctrl:1
	v_cndmask_b32_e32 v178, v178, v180, vcc
	v_cndmask_b32_e32 v180, v180, v181, vcc
	v_cndmask_b32_e32 v181, v181, v182, vcc
	v_cndmask_b32_e32 v182, v182, v183, vcc
	v_cndmask_b32_e32 v183, v183, v184, vcc
	v_cndmask_b32_e32 v184, v184, v185, vcc
	v_cndmask_b32_e32 v185, v185, v179, vcc
	v_cndmask_b32_e32 v179, v179, v237, vcc
	v_cmp_eq_u32_e32 vcc, v186, v173
	v_max_i32_dpp v174, v174, v174 row_ror:8 row_mask:0xf bank_mask:0xf bound_ctrl:1
	v_max_i32_dpp v175, v175, v175 row_ror:4 row_mask:0xf bank_mask:0xf bound_ctrl:1
	v_cndmask_b32_e32 v186, v186, v187, vcc
	v_cndmask_b32_e32 v187, v187, v188, vcc
	v_cndmask_b32_e32 v188, v188, v190, vcc
	v_cndmask_b32_e32 v190, v190, v191, vcc
	v_cndmask_b32_e32 v191, v191, v192, vcc
	v_cndmask_b32_e32 v192, v192, v193, vcc
	v_cndmask_b32_e32 v193, v193, v189, vcc
	v_cndmask_b32_e32 v189, v189, v237, vcc
	v_cmp_eq_u32_e32 vcc, v194, v174
	v_max_i32_dpp v175, v175, v175 row_ror:8 row_mask:0xf bank_mask:0xf bound_ctrl:1
	s_nop 0
	v_cndmask_b32_e32 v194, v194, v195, vcc
	v_cndmask_b32_e32 v195, v195, v196, vcc
	v_cndmask_b32_e32 v196, v196, v197, vcc
	v_cndmask_b32_e32 v197, v197, v199, vcc
	v_cndmask_b32_e32 v199, v199, v203, vcc
	v_cndmask_b32_e32 v203, v203, v204, vcc
	v_cndmask_b32_e32 v204, v204, v198, vcc
	v_cndmask_b32_e32 v198, v198, v237, vcc
	v_cmp_eq_u32_e32 vcc, v205, v175
	s_nop 1
	v_cndmask_b32_e32 v205, v205, v207, vcc
	v_cndmask_b32_e32 v207, v207, v208, vcc
	v_cndmask_b32_e32 v208, v208, v209, vcc
	v_cndmask_b32_e32 v209, v209, v210, vcc
	v_cndmask_b32_e32 v210, v210, v176, vcc
	v_cndmask_b32_e32 v211, v176, v177, vcc
	v_max_i32_dpp v176, v178, v178 row_ror:1 row_mask:0xf bank_mask:0xf bound_ctrl:1
	v_cndmask_b32_e32 v212, v177, v206, vcc
	v_cndmask_b32_e32 v206, v206, v237, vcc
	v_max_i32_dpp v176, v176, v176 row_ror:2 row_mask:0xf bank_mask:0xf bound_ctrl:1
	v_max_i32_dpp v177, v186, v186 row_ror:1 row_mask:0xf bank_mask:0xf bound_ctrl:1
	s_nop 0
	v_max_i32_dpp v176, v176, v176 row_ror:4 row_mask:0xf bank_mask:0xf bound_ctrl:1
	v_max_i32_dpp v177, v177, v177 row_ror:2 row_mask:0xf bank_mask:0xf bound_ctrl:1
	s_nop 0
	v_max_i32_dpp v176, v176, v176 row_ror:8 row_mask:0xf bank_mask:0xf bound_ctrl:1
	v_cmp_eq_u32_e32 vcc, v178, v176
	v_max_i32_dpp v177, v177, v177 row_ror:4 row_mask:0xf bank_mask:0xf bound_ctrl:1
	s_nop 0
	v_cndmask_b32_e32 v213, v178, v180, vcc
	v_max_i32_dpp v178, v194, v194 row_ror:1 row_mask:0xf bank_mask:0xf bound_ctrl:1
	v_cndmask_b32_e32 v214, v180, v181, vcc
	v_cndmask_b32_e32 v181, v181, v182, vcc
	v_cndmask_b32_e32 v182, v182, v183, vcc
	v_cndmask_b32_e32 v183, v183, v184, vcc
	v_cndmask_b32_e32 v184, v184, v185, vcc
	v_cndmask_b32_e32 v185, v185, v179, vcc
	v_cndmask_b32_e32 v215, v179, v237, vcc
	v_max_i32_dpp v178, v178, v178 row_ror:2 row_mask:0xf bank_mask:0xf bound_ctrl:1
	v_max_i32_dpp v179, v205, v205 row_ror:1 row_mask:0xf bank_mask:0xf bound_ctrl:1
	v_max_i32_dpp v177, v177, v177 row_ror:8 row_mask:0xf bank_mask:0xf bound_ctrl:1
	v_max_i32_dpp v178, v178, v178 row_ror:4 row_mask:0xf bank_mask:0xf bound_ctrl:1
	v_max_i32_dpp v179, v179, v179 row_ror:2 row_mask:0xf bank_mask:0xf bound_ctrl:1
	v_max_i32_dpp v180, v213, v213 row_ror:1 row_mask:0xf bank_mask:0xf bound_ctrl:1
	v_cmp_eq_u32_e32 vcc, v186, v177
	v_max_i32_dpp v178, v178, v178 row_ror:8 row_mask:0xf bank_mask:0xf bound_ctrl:1
	v_max_i32_dpp v179, v179, v179 row_ror:4 row_mask:0xf bank_mask:0xf bound_ctrl:1
	v_max_i32_dpp v180, v180, v180 row_ror:2 row_mask:0xf bank_mask:0xf bound_ctrl:1
	v_cndmask_b32_e32 v186, v186, v187, vcc
	v_cndmask_b32_e32 v187, v187, v188, vcc
	v_cndmask_b32_e32 v188, v188, v190, vcc
	v_cndmask_b32_e32 v190, v190, v191, vcc
	v_cndmask_b32_e32 v191, v191, v192, vcc
	v_cndmask_b32_e32 v192, v192, v193, vcc
	v_cndmask_b32_e32 v193, v193, v189, vcc
	v_cndmask_b32_e32 v189, v189, v237, vcc
	v_cmp_eq_u32_e32 vcc, v194, v178
	v_max_i32_dpp v179, v179, v179 row_ror:8 row_mask:0xf bank_mask:0xf bound_ctrl:1
	v_max_i32_dpp v180, v180, v180 row_ror:4 row_mask:0xf bank_mask:0xf bound_ctrl:1
	v_cndmask_b32_e32 v194, v194, v195, vcc
	v_cndmask_b32_e32 v195, v195, v196, vcc
	v_cndmask_b32_e32 v196, v196, v197, vcc
	v_cndmask_b32_e32 v197, v197, v199, vcc
	v_cndmask_b32_e32 v199, v199, v203, vcc
	v_cndmask_b32_e32 v203, v203, v204, vcc
	v_cndmask_b32_e32 v204, v204, v198, vcc
	v_cndmask_b32_e32 v198, v198, v237, vcc
	v_cmp_eq_u32_e32 vcc, v205, v179
	v_max_i32_dpp v180, v180, v180 row_ror:8 row_mask:0xf bank_mask:0xf bound_ctrl:1
	s_nop 0
	v_cndmask_b32_e32 v205, v205, v207, vcc
	v_cndmask_b32_e32 v207, v207, v208, vcc
	v_cndmask_b32_e32 v208, v208, v209, vcc
	v_cndmask_b32_e32 v209, v209, v210, vcc
	v_cndmask_b32_e32 v210, v210, v211, vcc
	v_cndmask_b32_e32 v211, v211, v212, vcc
	v_cndmask_b32_e32 v212, v212, v206, vcc
	v_cndmask_b32_e32 v206, v206, v237, vcc
	v_cmp_eq_u32_e32 vcc, v213, v180
	s_nop 1
	v_cndmask_b32_e32 v213, v213, v214, vcc
	v_cndmask_b32_e32 v214, v214, v181, vcc
	v_cndmask_b32_e32 v216, v181, v182, vcc
	v_max_i32_dpp v181, v186, v186 row_ror:1 row_mask:0xf bank_mask:0xf bound_ctrl:1
	v_cndmask_b32_e32 v217, v182, v183, vcc
	v_max_i32_dpp v182, v194, v194 row_ror:1 row_mask:0xf bank_mask:0xf bound_ctrl:1
	v_max_i32_dpp v181, v181, v181 row_ror:2 row_mask:0xf bank_mask:0xf bound_ctrl:1
	v_cndmask_b32_e32 v218, v183, v184, vcc
	v_max_i32_dpp v182, v182, v182 row_ror:2 row_mask:0xf bank_mask:0xf bound_ctrl:1
	v_max_i32_dpp v181, v181, v181 row_ror:4 row_mask:0xf bank_mask:0xf bound_ctrl:1
	v_max_i32_dpp v183, v205, v205 row_ror:1 row_mask:0xf bank_mask:0xf bound_ctrl:1
	v_cndmask_b32_e32 v219, v184, v185, vcc
	v_max_i32_dpp v181, v181, v181 row_ror:8 row_mask:0xf bank_mask:0xf bound_ctrl:1
	v_max_i32_dpp v182, v182, v182 row_ror:4 row_mask:0xf bank_mask:0xf bound_ctrl:1
	v_max_i32_dpp v183, v183, v183 row_ror:2 row_mask:0xf bank_mask:0xf bound_ctrl:1
	v_max_i32_dpp v184, v213, v213 row_ror:1 row_mask:0xf bank_mask:0xf bound_ctrl:1
	v_cndmask_b32_e32 v185, v185, v215, vcc
	v_cndmask_b32_e32 v215, v215, v237, vcc
	v_cmp_eq_u32_e32 vcc, v186, v181
	v_max_i32_dpp v182, v182, v182 row_ror:8 row_mask:0xf bank_mask:0xf bound_ctrl:1
	v_max_i32_dpp v183, v183, v183 row_ror:4 row_mask:0xf bank_mask:0xf bound_ctrl:1
	v_max_i32_dpp v184, v184, v184 row_ror:2 row_mask:0xf bank_mask:0xf bound_ctrl:1
	v_cndmask_b32_e32 v186, v186, v187, vcc
	v_cndmask_b32_e32 v187, v187, v188, vcc
	v_cndmask_b32_e32 v188, v188, v190, vcc
	v_cndmask_b32_e32 v190, v190, v191, vcc
	v_cndmask_b32_e32 v191, v191, v192, vcc
	v_cndmask_b32_e32 v192, v192, v193, vcc
	v_cndmask_b32_e32 v193, v193, v189, vcc
	v_cndmask_b32_e32 v189, v189, v237, vcc
	v_cmp_eq_u32_e32 vcc, v194, v182
	v_max_i32_dpp v183, v183, v183 row_ror:8 row_mask:0xf bank_mask:0xf bound_ctrl:1
	v_max_i32_dpp v184, v184, v184 row_ror:4 row_mask:0xf bank_mask:0xf bound_ctrl:1
	v_cndmask_b32_e32 v194, v194, v195, vcc
	v_cndmask_b32_e32 v195, v195, v196, vcc
	v_cndmask_b32_e32 v196, v196, v197, vcc
	v_cndmask_b32_e32 v197, v197, v199, vcc
	v_cndmask_b32_e32 v199, v199, v203, vcc
	v_cndmask_b32_e32 v203, v203, v204, vcc
	v_cndmask_b32_e32 v204, v204, v198, vcc
	v_cndmask_b32_e32 v198, v198, v237, vcc
	v_cmp_eq_u32_e32 vcc, v205, v183
	v_max_i32_dpp v184, v184, v184 row_ror:8 row_mask:0xf bank_mask:0xf bound_ctrl:1
	s_nop 0
	v_cndmask_b32_e32 v205, v205, v207, vcc
	v_cndmask_b32_e32 v207, v207, v208, vcc
	v_cndmask_b32_e32 v208, v208, v209, vcc
	v_cndmask_b32_e32 v209, v209, v210, vcc
	v_cndmask_b32_e32 v210, v210, v211, vcc
	v_cndmask_b32_e32 v211, v211, v212, vcc
	v_cndmask_b32_e32 v212, v212, v206, vcc
	v_cndmask_b32_e32 v206, v206, v237, vcc
	v_cmp_eq_u32_e32 vcc, v213, v184
	s_nop 1
	v_cndmask_b32_e32 v213, v213, v214, vcc
	v_cndmask_b32_e32 v214, v214, v216, vcc
	v_cndmask_b32_e32 v216, v216, v217, vcc
	v_cndmask_b32_e32 v217, v217, v218, vcc
	v_cndmask_b32_e32 v218, v218, v219, vcc
	v_cndmask_b32_e32 v219, v219, v185, vcc
	v_cndmask_b32_e32 v220, v185, v215, vcc
	v_max_i32_dpp v185, v186, v186 row_ror:1 row_mask:0xf bank_mask:0xf bound_ctrl:1
	v_cndmask_b32_e32 v215, v215, v237, vcc
	s_nop 0
	v_max_i32_dpp v185, v185, v185 row_ror:2 row_mask:0xf bank_mask:0xf bound_ctrl:1
	s_nop 1
	v_max_i32_dpp v185, v185, v185 row_ror:4 row_mask:0xf bank_mask:0xf bound_ctrl:1
	s_nop 1
	v_max_i32_dpp v185, v185, v185 row_ror:8 row_mask:0xf bank_mask:0xf bound_ctrl:1
	v_cmp_eq_u32_e32 vcc, v186, v185
	s_nop 1
	v_cndmask_b32_e32 v221, v186, v187, vcc
	v_max_i32_dpp v186, v194, v194 row_ror:1 row_mask:0xf bank_mask:0xf bound_ctrl:1
	v_cndmask_b32_e32 v222, v187, v188, vcc
	v_max_i32_dpp v187, v205, v205 row_ror:1 row_mask:0xf bank_mask:0xf bound_ctrl:1
	v_max_i32_dpp v186, v186, v186 row_ror:2 row_mask:0xf bank_mask:0xf bound_ctrl:1
	v_cndmask_b32_e32 v223, v188, v190, vcc
	v_max_i32_dpp v187, v187, v187 row_ror:2 row_mask:0xf bank_mask:0xf bound_ctrl:1
	v_max_i32_dpp v186, v186, v186 row_ror:4 row_mask:0xf bank_mask:0xf bound_ctrl:1
	v_max_i32_dpp v188, v213, v213 row_ror:1 row_mask:0xf bank_mask:0xf bound_ctrl:1
	v_cndmask_b32_e32 v190, v190, v191, vcc
	v_cndmask_b32_e32 v191, v191, v192, vcc
	v_cndmask_b32_e32 v192, v192, v193, vcc
	v_cndmask_b32_e32 v193, v193, v189, vcc
	v_max_i32_dpp v186, v186, v186 row_ror:8 row_mask:0xf bank_mask:0xf bound_ctrl:1
	v_max_i32_dpp v187, v187, v187 row_ror:4 row_mask:0xf bank_mask:0xf bound_ctrl:1
	v_max_i32_dpp v188, v188, v188 row_ror:2 row_mask:0xf bank_mask:0xf bound_ctrl:1
	v_max_i32_dpp v189, v221, v221 row_ror:1 row_mask:0xf bank_mask:0xf bound_ctrl:1
	v_cmp_eq_u32_e32 vcc, v194, v186
	v_max_i32_dpp v187, v187, v187 row_ror:8 row_mask:0xf bank_mask:0xf bound_ctrl:1
	v_max_i32_dpp v188, v188, v188 row_ror:4 row_mask:0xf bank_mask:0xf bound_ctrl:1
	v_max_i32_dpp v189, v189, v189 row_ror:2 row_mask:0xf bank_mask:0xf bound_ctrl:1
	v_cndmask_b32_e32 v194, v194, v195, vcc
	v_cndmask_b32_e32 v195, v195, v196, vcc
	v_cndmask_b32_e32 v196, v196, v197, vcc
	v_cndmask_b32_e32 v197, v197, v199, vcc
	v_cndmask_b32_e32 v199, v199, v203, vcc
	v_cndmask_b32_e32 v203, v203, v204, vcc
	v_cndmask_b32_e32 v198, v204, v198, vcc
	v_cmp_eq_u32_e32 vcc, v205, v187
	v_max_i32_dpp v188, v188, v188 row_ror:8 row_mask:0xf bank_mask:0xf bound_ctrl:1
	v_max_i32_dpp v189, v189, v189 row_ror:4 row_mask:0xf bank_mask:0xf bound_ctrl:1
	v_cndmask_b32_e32 v204, v205, v207, vcc
	v_cndmask_b32_e32 v205, v207, v208, vcc
	v_cndmask_b32_e32 v207, v208, v209, vcc
	v_cndmask_b32_e32 v208, v209, v210, vcc
	v_cndmask_b32_e32 v209, v210, v211, vcc
	v_cndmask_b32_e32 v210, v211, v212, vcc
	v_cndmask_b32_e32 v206, v212, v206, vcc
	v_cmp_eq_u32_e32 vcc, v213, v188
	v_max_i32_dpp v189, v189, v189 row_ror:8 row_mask:0xf bank_mask:0xf bound_ctrl:1
	s_nop 0
	v_cndmask_b32_e32 v211, v213, v214, vcc
	v_cndmask_b32_e32 v212, v214, v216, vcc
	v_cndmask_b32_e32 v213, v216, v217, vcc
	v_cndmask_b32_e32 v214, v217, v218, vcc
	v_cndmask_b32_e32 v216, v218, v219, vcc
	v_cndmask_b32_e32 v217, v219, v220, vcc
	v_cndmask_b32_e32 v215, v220, v215, vcc
	v_cmp_eq_u32_e32 vcc, v221, v189
	s_nop 1
	v_cndmask_b32_e32 v218, v221, v222, vcc
	v_cndmask_b32_e32 v220, v223, v190, vcc
	v_cndmask_b32_e32 v221, v190, v191, vcc
	v_max_i32_dpp v190, v194, v194 row_ror:1 row_mask:0xf bank_mask:0xf bound_ctrl:1
	v_cndmask_b32_e32 v219, v222, v223, vcc
	v_cndmask_b32_e32 v222, v191, v192, vcc
	v_max_i32_dpp v190, v190, v190 row_ror:2 row_mask:0xf bank_mask:0xf bound_ctrl:1
	v_max_i32_dpp v191, v204, v204 row_ror:1 row_mask:0xf bank_mask:0xf bound_ctrl:1
	v_cndmask_b32_e32 v223, v192, v193, vcc
	v_max_i32_dpp v190, v190, v190 row_ror:4 row_mask:0xf bank_mask:0xf bound_ctrl:1
	v_max_i32_dpp v191, v191, v191 row_ror:2 row_mask:0xf bank_mask:0xf bound_ctrl:1
	v_max_i32_dpp v192, v211, v211 row_ror:1 row_mask:0xf bank_mask:0xf bound_ctrl:1
	v_max_i32_dpp v190, v190, v190 row_ror:8 row_mask:0xf bank_mask:0xf bound_ctrl:1
	v_cmp_eq_u32_e32 vcc, v194, v190
	v_max_i32_dpp v191, v191, v191 row_ror:4 row_mask:0xf bank_mask:0xf bound_ctrl:1
	v_max_i32_dpp v192, v192, v192 row_ror:2 row_mask:0xf bank_mask:0xf bound_ctrl:1
	v_cndmask_b32_e32 v224, v194, v195, vcc
	v_max_i32_dpp v193, v218, v218 row_ror:1 row_mask:0xf bank_mask:0xf bound_ctrl:1
	v_max_i32_dpp v191, v191, v191 row_ror:8 row_mask:0xf bank_mask:0xf bound_ctrl:1
	v_max_i32_dpp v192, v192, v192 row_ror:4 row_mask:0xf bank_mask:0xf bound_ctrl:1
	v_max_i32_dpp v193, v193, v193 row_ror:2 row_mask:0xf bank_mask:0xf bound_ctrl:1
	v_max_i32_dpp v194, v224, v224 row_ror:1 row_mask:0xf bank_mask:0xf bound_ctrl:1
	v_cndmask_b32_e32 v195, v195, v196, vcc
	v_cndmask_b32_e32 v196, v196, v197, vcc
	v_cndmask_b32_e32 v197, v197, v199, vcc
	v_cndmask_b32_e32 v199, v199, v203, vcc
	v_cndmask_b32_e32 v198, v203, v198, vcc
	v_cmp_eq_u32_e32 vcc, v204, v191
	v_max_i32_dpp v192, v192, v192 row_ror:8 row_mask:0xf bank_mask:0xf bound_ctrl:1
	v_max_i32_dpp v193, v193, v193 row_ror:4 row_mask:0xf bank_mask:0xf bound_ctrl:1
	v_max_i32_dpp v194, v194, v194 row_ror:2 row_mask:0xf bank_mask:0xf bound_ctrl:1
	v_cndmask_b32_e32 v203, v204, v205, vcc
	v_cndmask_b32_e32 v204, v205, v207, vcc
	v_cndmask_b32_e32 v205, v207, v208, vcc
	v_cndmask_b32_e32 v207, v208, v209, vcc
	v_cndmask_b32_e32 v208, v209, v210, vcc
	v_cndmask_b32_e32 v206, v210, v206, vcc
	v_cmp_eq_u32_e32 vcc, v211, v192
	v_max_i32_dpp v193, v193, v193 row_ror:8 row_mask:0xf bank_mask:0xf bound_ctrl:1
	v_max_i32_dpp v194, v194, v194 row_ror:4 row_mask:0xf bank_mask:0xf bound_ctrl:1
	v_cndmask_b32_e32 v209, v211, v212, vcc
	v_cndmask_b32_e32 v210, v212, v213, vcc
	v_cndmask_b32_e32 v211, v213, v214, vcc
	v_cndmask_b32_e32 v212, v214, v216, vcc
	v_cndmask_b32_e32 v213, v216, v217, vcc
	v_cndmask_b32_e32 v214, v217, v215, vcc
	v_cmp_eq_u32_e32 vcc, v218, v193
	v_max_i32_dpp v194, v194, v194 row_ror:8 row_mask:0xf bank_mask:0xf bound_ctrl:1
	s_nop 0
	v_cndmask_b32_e32 v215, v218, v219, vcc
	v_cndmask_b32_e32 v216, v219, v220, vcc
	v_cndmask_b32_e32 v217, v220, v221, vcc
	v_cndmask_b32_e32 v218, v221, v222, vcc
	v_cndmask_b32_e32 v219, v222, v223, vcc
	v_cmp_eq_u32_e32 vcc, v224, v194
	s_nop 1
	v_cndmask_b32_e32 v220, v224, v195, vcc
	v_cndmask_b32_e32 v221, v195, v196, vcc
	v_max_i32_dpp v195, v203, v203 row_ror:1 row_mask:0xf bank_mask:0xf bound_ctrl:1
	v_cndmask_b32_e32 v222, v196, v197, vcc
	v_max_i32_dpp v196, v209, v209 row_ror:1 row_mask:0xf bank_mask:0xf bound_ctrl:1
	v_max_i32_dpp v195, v195, v195 row_ror:2 row_mask:0xf bank_mask:0xf bound_ctrl:1
	v_cndmask_b32_e32 v223, v197, v199, vcc
	v_max_i32_dpp v196, v196, v196 row_ror:2 row_mask:0xf bank_mask:0xf bound_ctrl:1
	v_max_i32_dpp v195, v195, v195 row_ror:4 row_mask:0xf bank_mask:0xf bound_ctrl:1
	v_max_i32_dpp v197, v215, v215 row_ror:1 row_mask:0xf bank_mask:0xf bound_ctrl:1
	v_cndmask_b32_e32 v199, v199, v198, vcc
	v_max_i32_dpp v195, v195, v195 row_ror:8 row_mask:0xf bank_mask:0xf bound_ctrl:1
	v_max_i32_dpp v196, v196, v196 row_ror:4 row_mask:0xf bank_mask:0xf bound_ctrl:1
	v_max_i32_dpp v197, v197, v197 row_ror:2 row_mask:0xf bank_mask:0xf bound_ctrl:1
	v_max_i32_dpp v198, v220, v220 row_ror:1 row_mask:0xf bank_mask:0xf bound_ctrl:1
	v_cmp_eq_u32_e32 vcc, v203, v195
	v_max_i32_dpp v196, v196, v196 row_ror:8 row_mask:0xf bank_mask:0xf bound_ctrl:1
	v_max_i32_dpp v197, v197, v197 row_ror:4 row_mask:0xf bank_mask:0xf bound_ctrl:1
	v_max_i32_dpp v198, v198, v198 row_ror:2 row_mask:0xf bank_mask:0xf bound_ctrl:1
	v_cndmask_b32_e32 v203, v203, v204, vcc
	v_cndmask_b32_e32 v204, v204, v205, vcc
	v_cndmask_b32_e32 v205, v205, v207, vcc
	v_cndmask_b32_e32 v207, v207, v208, vcc
	v_cndmask_b32_e32 v206, v208, v206, vcc
	v_cmp_eq_u32_e32 vcc, v209, v196
	v_max_i32_dpp v197, v197, v197 row_ror:8 row_mask:0xf bank_mask:0xf bound_ctrl:1
	v_max_i32_dpp v198, v198, v198 row_ror:4 row_mask:0xf bank_mask:0xf bound_ctrl:1
	v_cndmask_b32_e32 v208, v209, v210, vcc
	v_cndmask_b32_e32 v209, v210, v211, vcc
	v_cndmask_b32_e32 v210, v211, v212, vcc
	v_cndmask_b32_e32 v211, v212, v213, vcc
	v_cndmask_b32_e32 v212, v213, v214, vcc
	v_cmp_eq_u32_e32 vcc, v215, v197
	v_max_i32_dpp v198, v198, v198 row_ror:8 row_mask:0xf bank_mask:0xf bound_ctrl:1
	s_nop 0
	v_cndmask_b32_e32 v213, v215, v216, vcc
	v_cndmask_b32_e32 v214, v216, v217, vcc
	v_cndmask_b32_e32 v215, v217, v218, vcc
	v_cndmask_b32_e32 v216, v218, v219, vcc
	v_cmp_eq_u32_e32 vcc, v220, v198
	s_nop 1
	v_cndmask_b32_e32 v217, v220, v221, vcc
	v_cndmask_b32_e32 v220, v223, v199, vcc
	v_max_i32_dpp v199, v203, v203 row_ror:1 row_mask:0xf bank_mask:0xf bound_ctrl:1
	v_cndmask_b32_e32 v218, v221, v222, vcc
	v_cndmask_b32_e32 v219, v222, v223, vcc
	v_max_i32_dpp v199, v199, v199 row_ror:2 row_mask:0xf bank_mask:0xf bound_ctrl:1
	s_nop 1
	v_max_i32_dpp v199, v199, v199 row_ror:4 row_mask:0xf bank_mask:0xf bound_ctrl:1
	s_nop 1
	v_max_i32_dpp v199, v199, v199 row_ror:8 row_mask:0xf bank_mask:0xf bound_ctrl:1
	v_cmp_eq_u32_e32 vcc, v203, v199
	s_nop 1
	v_cndmask_b32_e32 v221, v203, v204, vcc
	v_max_i32_dpp v203, v208, v208 row_ror:1 row_mask:0xf bank_mask:0xf bound_ctrl:1
	v_cndmask_b32_e32 v222, v207, v206, vcc
	v_max_i32_dpp v206, v213, v213 row_ror:1 row_mask:0xf bank_mask:0xf bound_ctrl:1
	v_max_i32_dpp v203, v203, v203 row_ror:2 row_mask:0xf bank_mask:0xf bound_ctrl:1
	v_cndmask_b32_e32 v204, v204, v205, vcc
	v_cndmask_b32_e32 v205, v205, v207, vcc
	v_max_i32_dpp v203, v203, v203 row_ror:4 row_mask:0xf bank_mask:0xf bound_ctrl:1
	v_max_i32_dpp v206, v206, v206 row_ror:2 row_mask:0xf bank_mask:0xf bound_ctrl:1
	v_max_i32_dpp v207, v217, v217 row_ror:1 row_mask:0xf bank_mask:0xf bound_ctrl:1
	v_max_i32_dpp v203, v203, v203 row_ror:8 row_mask:0xf bank_mask:0xf bound_ctrl:1
	v_cmp_eq_u32_e32 vcc, v208, v203
	v_max_i32_dpp v206, v206, v206 row_ror:4 row_mask:0xf bank_mask:0xf bound_ctrl:1
	v_max_i32_dpp v207, v207, v207 row_ror:2 row_mask:0xf bank_mask:0xf bound_ctrl:1
	v_cndmask_b32_e32 v223, v208, v209, vcc
	v_max_i32_dpp v208, v221, v221 row_ror:1 row_mask:0xf bank_mask:0xf bound_ctrl:1
	v_cndmask_b32_e32 v224, v209, v210, vcc
	v_max_i32_dpp v206, v206, v206 row_ror:8 row_mask:0xf bank_mask:0xf bound_ctrl:1
	v_max_i32_dpp v207, v207, v207 row_ror:4 row_mask:0xf bank_mask:0xf bound_ctrl:1
	v_max_i32_dpp v208, v208, v208 row_ror:2 row_mask:0xf bank_mask:0xf bound_ctrl:1
	v_max_i32_dpp v209, v223, v223 row_ror:1 row_mask:0xf bank_mask:0xf bound_ctrl:1
	v_cndmask_b32_e32 v210, v210, v211, vcc
	v_cndmask_b32_e32 v211, v211, v212, vcc
	v_cmp_eq_u32_e32 vcc, v213, v206
	v_max_i32_dpp v207, v207, v207 row_ror:8 row_mask:0xf bank_mask:0xf bound_ctrl:1
	v_max_i32_dpp v208, v208, v208 row_ror:4 row_mask:0xf bank_mask:0xf bound_ctrl:1
	v_max_i32_dpp v209, v209, v209 row_ror:2 row_mask:0xf bank_mask:0xf bound_ctrl:1
	v_cndmask_b32_e32 v212, v213, v214, vcc
	v_cndmask_b32_e32 v213, v214, v215, vcc
	v_cndmask_b32_e32 v214, v215, v216, vcc
	v_cmp_eq_u32_e32 vcc, v217, v207
	v_max_i32_dpp v208, v208, v208 row_ror:8 row_mask:0xf bank_mask:0xf bound_ctrl:1
	v_max_i32_dpp v209, v209, v209 row_ror:4 row_mask:0xf bank_mask:0xf bound_ctrl:1
	v_cndmask_b32_e32 v215, v217, v218, vcc
	v_cndmask_b32_e32 v216, v218, v219, vcc
	v_cndmask_b32_e32 v217, v219, v220, vcc
	v_cmp_eq_u32_e32 vcc, v221, v208
	v_max_i32_dpp v209, v209, v209 row_ror:8 row_mask:0xf bank_mask:0xf bound_ctrl:1
	s_nop 0
	v_cndmask_b32_e32 v218, v221, v204, vcc
	v_cndmask_b32_e32 v204, v204, v205, vcc
	v_cndmask_b32_e32 v205, v205, v222, vcc
	v_cmp_eq_u32_e32 vcc, v223, v209
	s_nop 1
	v_cndmask_b32_e32 v220, v224, v210, vcc
	v_cndmask_b32_e32 v221, v210, v211, vcc
	v_max_i32_dpp v210, v212, v212 row_ror:1 row_mask:0xf bank_mask:0xf bound_ctrl:1
	v_cndmask_b32_e32 v219, v223, v224, vcc
	v_max_i32_dpp v211, v215, v215 row_ror:1 row_mask:0xf bank_mask:0xf bound_ctrl:1
	v_max_i32_dpp v210, v210, v210 row_ror:2 row_mask:0xf bank_mask:0xf bound_ctrl:1
	s_nop 0
	v_max_i32_dpp v211, v211, v211 row_ror:2 row_mask:0xf bank_mask:0xf bound_ctrl:1
	v_max_i32_dpp v210, v210, v210 row_ror:4 row_mask:0xf bank_mask:0xf bound_ctrl:1
	s_nop 0
	v_max_i32_dpp v211, v211, v211 row_ror:4 row_mask:0xf bank_mask:0xf bound_ctrl:1
	v_max_i32_dpp v210, v210, v210 row_ror:8 row_mask:0xf bank_mask:0xf bound_ctrl:1
	v_cmp_eq_u32_e32 vcc, v212, v210
	v_max_i32_dpp v211, v211, v211 row_ror:8 row_mask:0xf bank_mask:0xf bound_ctrl:1
	s_nop 0
	v_cndmask_b32_e32 v222, v212, v213, vcc
	v_max_i32_dpp v212, v218, v218 row_ror:1 row_mask:0xf bank_mask:0xf bound_ctrl:1
	v_cndmask_b32_e32 v223, v213, v214, vcc
	v_cmp_eq_u32_e32 vcc, v215, v211
	v_max_i32_dpp v212, v212, v212 row_ror:2 row_mask:0xf bank_mask:0xf bound_ctrl:1
	v_max_i32_dpp v214, v222, v222 row_ror:1 row_mask:0xf bank_mask:0xf bound_ctrl:1
	v_cndmask_b32_e32 v224, v215, v216, vcc
	v_max_i32_dpp v212, v212, v212 row_ror:4 row_mask:0xf bank_mask:0xf bound_ctrl:1
	v_cndmask_b32_e32 v216, v216, v217, vcc
	v_max_i32_dpp v214, v214, v214 row_ror:2 row_mask:0xf bank_mask:0xf bound_ctrl:1
	v_max_i32_dpp v212, v212, v212 row_ror:8 row_mask:0xf bank_mask:0xf bound_ctrl:1
	v_cmp_eq_u32_e32 vcc, v218, v212
	v_max_i32_dpp v215, v224, v224 row_ror:1 row_mask:0xf bank_mask:0xf bound_ctrl:1
	v_max_i32_dpp v214, v214, v214 row_ror:4 row_mask:0xf bank_mask:0xf bound_ctrl:1
	v_cndmask_b32_e32 v217, v218, v204, vcc
	v_cndmask_b32_e32 v204, v204, v205, vcc
	v_max_i32_dpp v205, v219, v219 row_ror:1 row_mask:0xf bank_mask:0xf bound_ctrl:1
	v_max_i32_dpp v215, v215, v215 row_ror:2 row_mask:0xf bank_mask:0xf bound_ctrl:1
	v_max_i32_dpp v214, v214, v214 row_ror:8 row_mask:0xf bank_mask:0xf bound_ctrl:1
	v_max_i32_dpp v205, v205, v205 row_ror:2 row_mask:0xf bank_mask:0xf bound_ctrl:1
	v_max_i32_dpp v215, v215, v215 row_ror:4 row_mask:0xf bank_mask:0xf bound_ctrl:1
	s_nop 0
	v_max_i32_dpp v205, v205, v205 row_ror:4 row_mask:0xf bank_mask:0xf bound_ctrl:1
	v_max_i32_dpp v215, v215, v215 row_ror:8 row_mask:0xf bank_mask:0xf bound_ctrl:1
	s_nop 0
	v_max_i32_dpp v213, v205, v205 row_ror:8 row_mask:0xf bank_mask:0xf bound_ctrl:1
	v_cmp_eq_u32_e32 vcc, v219, v213
	s_nop 1
	v_cndmask_b32_e32 v205, v219, v220, vcc
	v_cndmask_b32_e32 v218, v220, v221, vcc
	v_cmp_eq_u32_e32 vcc, v222, v214
	v_mov_b32_e32 v221, v201
	s_nop 0
	v_cndmask_b32_e32 v219, v222, v223, vcc
	v_cmp_eq_u32_e32 vcc, v224, v215
	v_mov_b32_e32 v223, v201
	s_nop 0
	v_cndmask_b32_e32 v220, v224, v216, vcc
	v_max_i32_dpp v216, v217, v217 row_ror:1 row_mask:0xf bank_mask:0xf bound_ctrl:1
	s_nop 0
	v_max_i32_dpp v220, v220, v220 row_ror:1 row_mask:0xf bank_mask:0xf bound_ctrl:1
	v_max_i32_dpp v216, v216, v216 row_ror:2 row_mask:0xf bank_mask:0xf bound_ctrl:1
	s_nop 0
	v_max_i32_dpp v220, v220, v220 row_ror:2 row_mask:0xf bank_mask:0xf bound_ctrl:1
	v_max_i32_dpp v216, v216, v216 row_ror:4 row_mask:0xf bank_mask:0xf bound_ctrl:1
	s_nop 0
	v_max_i32_dpp v220, v220, v220 row_ror:4 row_mask:0xf bank_mask:0xf bound_ctrl:1
	v_max_i32_dpp v216, v216, v216 row_ror:8 row_mask:0xf bank_mask:0xf bound_ctrl:1
	v_cmp_eq_u32_e32 vcc, v217, v216
	v_mov_b32_dpp v221, v220 row_ror:8 row_mask:0xf bank_mask:0xf
	s_nop 0
	v_cndmask_b32_e32 v204, v217, v204, vcc
	v_max_i32_dpp v217, v205, v205 row_ror:1 row_mask:0xf bank_mask:0xf bound_ctrl:1
	s_nop 0
	v_max_i32_dpp v204, v204, v204 row_ror:1 row_mask:0xf bank_mask:0xf bound_ctrl:1
	v_max_i32_dpp v217, v217, v217 row_ror:2 row_mask:0xf bank_mask:0xf bound_ctrl:1
	s_nop 0
	v_max_i32_dpp v204, v204, v204 row_ror:2 row_mask:0xf bank_mask:0xf bound_ctrl:1
	v_max_i32_dpp v217, v217, v217 row_ror:4 row_mask:0xf bank_mask:0xf bound_ctrl:1
	s_nop 0
	v_max_i32_dpp v240, v204, v204 row_ror:4 row_mask:0xf bank_mask:0xf bound_ctrl:1
	v_max_i32_dpp v217, v217, v217 row_ror:8 row_mask:0xf bank_mask:0xf bound_ctrl:1
	v_cmp_eq_u32_e32 vcc, v205, v217
	v_mov_b32_dpp v241, v240 row_ror:8 row_mask:0xf bank_mask:0xf
	s_nop 0
	v_cndmask_b32_e32 v205, v205, v218, vcc
	v_max_i32_dpp v218, v219, v219 row_ror:1 row_mask:0xf bank_mask:0xf bound_ctrl:1
	v_mov_b32_e32 v219, v201
	v_max_i32_dpp v204, v205, v205 row_ror:1 row_mask:0xf bank_mask:0xf bound_ctrl:1
	v_max_i32_dpp v218, v218, v218 row_ror:2 row_mask:0xf bank_mask:0xf bound_ctrl:1
	s_andn2_b64 vcc, exec, s[18:19]
	v_max_i32_dpp v204, v204, v204 row_ror:2 row_mask:0xf bank_mask:0xf bound_ctrl:1
	v_max_i32_dpp v218, v218, v218 row_ror:4 row_mask:0xf bank_mask:0xf bound_ctrl:1
	s_nop 0
	v_max_i32_dpp v222, v204, v204 row_ror:4 row_mask:0xf bank_mask:0xf bound_ctrl:1
	v_cndmask_b32_e64 v204, 0, 1, s[18:19]
	v_mov_b32_dpp v219, v218 row_ror:8 row_mask:0xf bank_mask:0xf
	v_cmp_ne_u32_e64 s[52:53], 1, v204
	v_mov_b32_dpp v223, v222 row_ror:8 row_mask:0xf bank_mask:0xf
	s_cbranch_vccnz .LBB0_1854
	v_lshl_add_u64 v[48:49], s[62:63], 0, v[110:111]
	global_load_dwordx4 v[32:35], v[48:49], off offset:48
	global_load_dwordx4 v[36:39], v[48:49], off offset:32
	global_load_dwordx4 v[40:43], v[48:49], off offset:16
	global_load_dwordx4 v[44:47], v[48:49], off
	v_lshl_add_u64 v[60:61], v[48:49], 0, s[60:61]
	v_add_co_u32_e32 v48, vcc, 0x1000, v48
	v_lshl_add_u64 v[80:81], s[68:69], 0, v[110:111]
	s_mov_b64 s[80:81], 0x8000000
	v_addc_co_u32_e32 v49, vcc, 0, v49, vcc
	v_lshl_add_u64 v[76:77], v[80:81], 0, s[80:81]
	s_brev_b32 s80, 16
	v_add_co_u32_e32 v64, vcc, s80, v80
	s_mov_b64 s[80:81], 0x8001000
	s_nop 0
	v_addc_co_u32_e32 v65, vcc, 0, v81, vcc
	v_lshl_add_u64 v[92:93], v[80:81], 0, s[80:81]
	v_add_co_u32_e32 v80, vcc, 0x8001000, v80
	global_load_dwordx4 v[48:51], v[48:49], off
	s_nop 0
	global_load_dwordx4 v[52:55], v[60:61], off offset:48
	global_load_dwordx4 v[56:59], v[60:61], off offset:32
	s_nop 0
	global_load_dwordx4 v[60:63], v[60:61], off offset:16
	v_addc_co_u32_e32 v81, vcc, 0, v81, vcc
	global_load_dwordx4 v[64:67], v[64:65], off
	s_nop 0
	global_load_dwordx4 v[68:71], v[76:77], off offset:48
	global_load_dwordx4 v[72:75], v[76:77], off offset:32
	s_nop 0
	global_load_dwordx4 v[76:79], v[76:77], off offset:16
	s_nop 0
	global_load_dwordx4 v[80:83], v[80:81], off
	s_nop 0
	global_load_dwordx4 v[84:87], v[92:93], off offset:48
	global_load_dwordx4 v[88:91], v[92:93], off offset:32
	s_nop 0
	global_load_dwordx4 v[92:95], v[92:93], off offset:16
.LBB0_1854:
	v_cndmask_b32_e64 v153, 0, v153, s[0:1]
	v_cndmask_b32_e64 v154, 0, v154, s[0:1]
	v_cndmask_b32_e64 v153, v153, v157, s[54:55]
	v_cndmask_b32_e64 v155, 0, v155, s[0:1]
	v_cndmask_b32_e64 v154, v154, v158, s[54:55]
	v_cndmask_b32_e64 v153, v153, v161, s[64:65]
	v_cndmask_b32_e64 v155, v155, v159, s[54:55]
	v_cndmask_b32_e64 v154, v154, v162, s[64:65]
	v_cndmask_b32_e64 v153, v153, v165, s[2:3]
	v_cndmask_b32_e64 v155, v155, v163, s[64:65]
	v_cndmask_b32_e64 v154, v154, v166, s[2:3]
	v_cndmask_b32_e64 v153, v153, v169, s[6:7]
	v_cndmask_b32_e64 v155, v155, v167, s[2:3]
	v_cndmask_b32_e64 v154, v154, v170, s[6:7]
	v_cndmask_b32_e64 v153, v153, v173, s[96:97]
	v_cndmask_b32_e64 v156, 0, v156, s[0:1]
	v_cndmask_b32_e64 v155, v155, v171, s[6:7]
	v_cndmask_b32_e64 v154, v154, v174, s[96:97]
	v_cndmask_b32_e64 v153, v153, v177, s[66:67]
	v_cndmask_b32_e64 v156, v156, v160, s[54:55]
	v_cndmask_b32_e64 v155, v155, v175, s[96:97]
	v_cndmask_b32_e64 v154, v154, v178, s[66:67]
	v_cndmask_b32_e64 v153, v153, v181, s[24:25]
	v_cndmask_b32_e64 v156, v156, v164, s[64:65]
	v_cndmask_b32_e64 v155, v155, v179, s[66:67]
	v_cndmask_b32_e64 v154, v154, v182, s[24:25]
	v_cndmask_b32_e64 v153, v153, v185, s[26:27]
	v_cndmask_b32_e64 v156, v156, v168, s[2:3]
	v_cndmask_b32_e64 v155, v155, v183, s[24:25]
	v_cndmask_b32_e64 v154, v154, v186, s[26:27]
	v_cndmask_b32_e64 v153, v153, v189, s[28:29]
	v_cndmask_b32_e64 v156, v156, v172, s[6:7]
	v_cndmask_b32_e64 v155, v155, v187, s[26:27]
	v_cndmask_b32_e64 v154, v154, v190, s[28:29]
	v_cndmask_b32_e64 v153, v153, v193, s[30:31]
	v_cndmask_b32_e64 v156, v156, v176, s[96:97]
	v_cndmask_b32_e64 v155, v155, v191, s[28:29]
	v_cndmask_b32_e64 v154, v154, v194, s[30:31]
	v_cndmask_b32_e64 v153, v153, v197, s[34:35]
	v_cndmask_b32_e64 v156, v156, v180, s[66:67]
	v_cndmask_b32_e64 v155, v155, v195, s[30:31]
	v_cndmask_b32_e64 v154, v154, v198, s[34:35]
	v_cndmask_b32_e64 v153, v153, v206, s[36:37]
	v_cndmask_b32_e64 v156, v156, v184, s[24:25]
	v_cndmask_b32_e64 v155, v155, v199, s[34:35]
	v_cndmask_b32_e64 v154, v154, v207, s[36:37]
	v_cndmask_b32_e64 v153, v153, v210, s[38:39]
	v_cndmask_b32_e64 v156, v156, v188, s[26:27]
	v_cndmask_b32_e64 v155, v155, v208, s[36:37]
	v_cndmask_b32_e64 v154, v154, v211, s[38:39]
	v_cndmask_b32_e64 v153, v153, v214, s[40:41]
	v_max_i32_e32 v157, v218, v219
	v_cndmask_b32_e64 v156, v156, v192, s[28:29]
	v_cndmask_b32_e64 v155, v155, v212, s[38:39]
	v_cndmask_b32_e64 v154, v154, v215, s[40:41]
	v_cndmask_b32_e64 v153, v153, v157, s[42:43]
	v_max_i32_e32 v157, v220, v221
	v_cndmask_b32_e64 v156, v156, v196, s[30:31]
	v_cndmask_b32_e64 v155, v155, v216, s[40:41]
	v_cndmask_b32_e64 v157, v154, v157, s[42:43]
	v_max_i32_e32 v154, v240, v241
	ds_bpermute_b32 v158, v146, v153
	v_cndmask_b32_e64 v156, v156, v203, s[34:35]
	v_cndmask_b32_e64 v159, v155, v154, s[42:43]
	ds_bpermute_b32 v154, v147, v153
	v_cndmask_b32_e64 v156, v156, v209, s[36:37]
	v_cndmask_b32_e64 v156, v156, v213, s[38:39]
	v_cndmask_b32_e64 v156, v156, v217, s[40:41]
	v_max_i32_e32 v155, v222, v223
	v_cndmask_b32_e64 v167, v156, v155, s[42:43]
	s_waitcnt lgkmcnt(1)
	v_lshlrev_b32_e32 v155, 7, v158
	v_and_b32_e32 v155, 0x3f80, v155
	s_waitcnt lgkmcnt(0)
	v_and_b32_e32 v156, 0x7f, v154
	s_movk_i32 s9, 0x3fff
	v_bitop3_b32 v184, v156, s9, v155 bitop3:0x36
	v_ashrrev_i32_e32 v155, 31, v154
	v_ashrrev_i32_e32 v156, 31, v158
	v_and_b32_e32 v155, 0x7fffffff, v155
	v_and_b32_e32 v156, 0x7fffffff, v156
	v_xor_b32_e32 v155, v155, v154
	v_xor_b32_e32 v154, v156, v158
	ds_bpermute_b32 v156, v148, v153
	ds_bpermute_b32 v153, v149, v153
	v_pk_add_f32 v[154:155], v[154:155], v[154:155] op_sel:[1,0] op_sel_hi:[0,1]
	s_movk_i32 s10, 0xffc0
	v_and_or_b32 v154, v154, s10, v141
	v_cndmask_b32_e64 v185, v238, v154, s[4:5]
	s_waitcnt lgkmcnt(1)
	v_lshlrev_b32_e32 v154, 7, v156
	v_and_b32_e32 v154, 0x3f80, v154
	s_waitcnt lgkmcnt(0)
	v_and_b32_e32 v155, 0x7f, v153
	v_bitop3_b32 v166, v155, s9, v154 bitop3:0x36
	v_ashrrev_i32_e32 v154, 31, v153
	v_ashrrev_i32_e32 v155, 31, v156
	v_and_b32_e32 v154, 0x7fffffff, v154
	v_and_b32_e32 v158, 0x7fffffff, v155
	v_xor_b32_e32 v155, v154, v153
	v_xor_b32_e32 v154, v158, v156
	v_pk_add_f32 v[154:155], v[154:155], v[154:155] op_sel:[1,0] op_sel_hi:[0,1]
	ds_bpermute_b32 v153, v146, v157
	ds_bpermute_b32 v155, v147, v157
	v_and_or_b32 v154, v154, s10, v141
	v_cndmask_b32_e64 v186, v238, v154, s[4:5]
	ds_bpermute_b32 v187, v149, v167
	s_waitcnt lgkmcnt(2)
	v_lshlrev_b32_e32 v154, 7, v153
	v_and_b32_e32 v154, 0x3f80, v154
	s_waitcnt lgkmcnt(1)
	v_and_b32_e32 v156, 0x7f, v155
	v_bitop3_b32 v164, v156, s9, v154 bitop3:0x36
	v_ashrrev_i32_e32 v154, 31, v155
	v_ashrrev_i32_e32 v156, 31, v153
	v_and_b32_e32 v154, 0x7fffffff, v154
	v_and_b32_e32 v156, 0x7fffffff, v156
	v_xor_b32_e32 v155, v154, v155
	v_xor_b32_e32 v154, v156, v153
	ds_bpermute_b32 v153, v148, v157
	v_pk_add_f32 v[154:155], v[154:155], v[154:155] op_sel:[1,0] op_sel_hi:[0,1]
	ds_bpermute_b32 v155, v149, v157
	v_and_or_b32 v154, v154, s10, v141
	v_cndmask_b32_e64 v165, v238, v154, s[4:5]
	s_waitcnt lgkmcnt(1)
	v_lshlrev_b32_e32 v154, 7, v153
	v_and_b32_e32 v154, 0x3f80, v154
	s_waitcnt lgkmcnt(0)
	v_and_b32_e32 v156, 0x7f, v155
	v_bitop3_b32 v162, v156, s9, v154 bitop3:0x36
	v_ashrrev_i32_e32 v154, 31, v155
	v_ashrrev_i32_e32 v156, 31, v153
	v_and_b32_e32 v154, 0x7fffffff, v154
	v_and_b32_e32 v156, 0x7fffffff, v156
	v_xor_b32_e32 v155, v154, v155
	v_xor_b32_e32 v154, v156, v153
	v_pk_add_f32 v[154:155], v[154:155], v[154:155] op_sel:[1,0] op_sel_hi:[0,1]
	ds_bpermute_b32 v153, v146, v159
	ds_bpermute_b32 v155, v147, v159
	v_and_or_b32 v154, v154, s10, v141
	v_cndmask_b32_e64 v163, v238, v154, s[4:5]
	ds_write2st64_b32 v142, v185, v186 offset1:1
	s_waitcnt lgkmcnt(2)
	v_lshlrev_b32_e32 v154, 7, v153
	v_and_b32_e32 v154, 0x3f80, v154
	s_waitcnt lgkmcnt(1)
	v_and_b32_e32 v156, 0x7f, v155
	v_bitop3_b32 v160, v156, s9, v154 bitop3:0x36
	v_ashrrev_i32_e32 v154, 31, v155
	v_ashrrev_i32_e32 v156, 31, v153
	v_and_b32_e32 v154, 0x7fffffff, v154
	v_and_b32_e32 v156, 0x7fffffff, v156
	v_xor_b32_e32 v155, v154, v155
	v_xor_b32_e32 v154, v156, v153
	ds_bpermute_b32 v153, v148, v159
	v_pk_add_f32 v[154:155], v[154:155], v[154:155] op_sel:[1,0] op_sel_hi:[0,1]
	ds_bpermute_b32 v155, v149, v159
	v_and_or_b32 v154, v154, s10, v141
	v_cndmask_b32_e64 v161, v238, v154, s[4:5]
	s_waitcnt lgkmcnt(1)
	v_lshlrev_b32_e32 v154, 7, v153
	v_and_b32_e32 v154, 0x3f80, v154
	s_waitcnt lgkmcnt(0)
	v_and_b32_e32 v156, 0x7f, v155
	v_bitop3_b32 v158, v156, s9, v154 bitop3:0x36
	v_ashrrev_i32_e32 v154, 31, v155
	v_ashrrev_i32_e32 v156, 31, v153
	v_and_b32_e32 v154, 0x7fffffff, v154
	v_and_b32_e32 v156, 0x7fffffff, v156
	v_xor_b32_e32 v155, v154, v155
	v_xor_b32_e32 v154, v156, v153
	ds_bpermute_b32 v153, v146, v167
	ds_bpermute_b32 v156, v147, v167
	v_pk_add_f32 v[154:155], v[154:155], v[154:155] op_sel:[1,0] op_sel_hi:[0,1]
	v_and_or_b32 v154, v154, s10, v141
	v_cndmask_b32_e64 v159, v238, v154, s[4:5]
	s_waitcnt lgkmcnt(1)
	v_lshlrev_b32_e32 v154, 7, v153
	v_and_b32_e32 v154, 0x3f80, v154
	s_waitcnt lgkmcnt(0)
	v_and_b32_e32 v155, 0x7f, v156
	v_bitop3_b32 v155, v155, s9, v154 bitop3:0x36
	v_ashrrev_i32_e32 v154, 31, v156
	v_ashrrev_i32_e32 v157, 31, v153
	ds_bpermute_b32 v167, v148, v167
	v_and_b32_e32 v154, 0x7fffffff, v154
	v_and_b32_e32 v168, 0x7fffffff, v157
	v_xor_b32_e32 v157, v154, v156
	v_xor_b32_e32 v156, v168, v153
	v_pk_add_f32 v[156:157], v[156:157], v[156:157] op_sel:[1,0] op_sel_hi:[0,1]
	v_and_or_b32 v153, v156, s10, v141
	v_cndmask_b32_e64 v157, v238, v153, s[4:5]
	v_ashrrev_i32_e32 v153, 31, v187
	s_waitcnt lgkmcnt(0)
	v_ashrrev_i32_e32 v154, 31, v167
	v_and_b32_e32 v153, 0x7fffffff, v153
	v_and_b32_e32 v154, 0x7fffffff, v154
	v_xor_b32_e32 v169, v153, v187
	v_xor_b32_e32 v168, v154, v167
	v_pk_add_f32 v[168:169], v[168:169], v[168:169] op_sel:[1,0] op_sel_hi:[0,1]
	v_and_or_b32 v153, v168, s10, v141
	v_cndmask_b32_e64 v153, v238, v153, s[4:5]
	ds_write2st64_b32 v142, v165, v163 offset0:2 offset1:3
	ds_write2st64_b32 v142, v161, v159 offset0:4 offset1:5
	ds_write2st64_b32 v142, v157, v153 offset0:6 offset1:7
	s_waitcnt lgkmcnt(0)
	v_mov_b32_e32 v154, s84
	ds_read_b128 v[168:171], v154
	v_lshlrev_b32_e32 v156, 7, v167
	ds_read_b128 v[172:175], v154 offset:16
	ds_read_b128 v[176:179], v154 offset:32
	ds_read_b128 v[180:183], v154 offset:48
	v_and_b32_e32 v156, 0x3f80, v156
	s_waitcnt lgkmcnt(3)
	v_cmp_gt_f32_e64 s[16:17], v169, v185
	v_cmp_gt_f32_e32 vcc, v168, v185
	v_cmp_gt_f32_e64 s[98:99], v170, v185
	v_cndmask_b32_e64 v167, 0, 1, s[16:17]
	v_addc_co_u32_e32 v167, vcc, 0, v167, vcc
	v_cmp_gt_f32_e32 vcc, v171, v185
	v_cndmask_b32_e64 v168, 0, 1, s[98:99]
	s_nop 0
	v_addc_co_u32_e32 v167, vcc, v167, v168, vcc
	s_waitcnt lgkmcnt(2)
	v_cmp_gt_f32_e64 s[16:17], v172, v185
	v_cmp_gt_f32_e32 vcc, v173, v185
	v_cmp_gt_f32_e64 s[98:99], v174, v185
	v_cndmask_b32_e64 v168, 0, 1, s[16:17]
	v_addc_co_u32_e32 v167, vcc, v167, v168, vcc
	v_cmp_gt_f32_e32 vcc, v175, v185
	v_cndmask_b32_e64 v168, 0, 1, s[98:99]
	s_nop 0
	v_addc_co_u32_e32 v167, vcc, v167, v168, vcc
	s_waitcnt lgkmcnt(1)
	v_cmp_gt_f32_e64 s[16:17], v176, v185
	v_cmp_gt_f32_e32 vcc, v177, v185
	v_cmp_gt_f32_e64 s[98:99], v178, v185
	v_cndmask_b32_e64 v168, 0, 1, s[16:17]
	v_addc_co_u32_e32 v167, vcc, v167, v168, vcc
	v_cmp_gt_f32_e32 vcc, v179, v185
	v_cndmask_b32_e64 v168, 0, 1, s[98:99]
	s_nop 0
	v_addc_co_u32_e32 v167, vcc, v167, v168, vcc
	s_waitcnt lgkmcnt(0)
	v_cmp_gt_f32_e64 s[16:17], v180, v185
	v_cmp_gt_f32_e32 vcc, v181, v185
	s_nop 0
	v_cndmask_b32_e64 v168, 0, 1, s[16:17]
	v_addc_co_u32_e32 v167, vcc, v167, v168, vcc
	ds_read_b128 v[168:171], v154 offset:64
	v_cmp_gt_f32_e64 s[16:17], v182, v185
	v_cmp_gt_f32_e32 vcc, v183, v185
	s_nop 0
	v_cndmask_b32_e64 v172, 0, 1, s[16:17]
	v_addc_co_u32_e32 v167, vcc, v167, v172, vcc
	ds_read_b128 v[172:175], v154 offset:80
	s_waitcnt lgkmcnt(1)
	v_cmp_gt_f32_e64 s[16:17], v168, v185
	v_cmp_gt_f32_e32 vcc, v169, v185
	v_cmp_gt_f32_e64 s[98:99], v170, v185
	v_cndmask_b32_e64 v168, 0, 1, s[16:17]
	v_addc_co_u32_e32 v167, vcc, v167, v168, vcc
	v_cmp_gt_f32_e32 vcc, v171, v185
	v_cndmask_b32_e64 v168, 0, 1, s[98:99]
	s_nop 0
	v_addc_co_u32_e32 v167, vcc, v167, v168, vcc
	s_waitcnt lgkmcnt(0)
	v_cmp_gt_f32_e64 s[16:17], v172, v185
	v_cmp_gt_f32_e32 vcc, v173, v185
	s_nop 0
	v_cndmask_b32_e64 v168, 0, 1, s[16:17]
	v_addc_co_u32_e32 v167, vcc, v167, v168, vcc
	ds_read_b128 v[168:171], v154 offset:96
	v_cmp_gt_f32_e64 s[16:17], v174, v185
	v_cmp_gt_f32_e32 vcc, v175, v185
	s_nop 0
	v_cndmask_b32_e64 v172, 0, 1, s[16:17]
	v_addc_co_u32_e32 v167, vcc, v167, v172, vcc
	ds_read_b128 v[172:175], v154 offset:112
	s_waitcnt lgkmcnt(1)
	v_cmp_gt_f32_e64 s[16:17], v168, v185
	v_cmp_gt_f32_e32 vcc, v169, v185
	v_cmp_gt_f32_e64 s[98:99], v170, v185
	v_cndmask_b32_e64 v168, 0, 1, s[16:17]
	v_addc_co_u32_e32 v167, vcc, v167, v168, vcc
	v_cmp_gt_f32_e32 vcc, v171, v185
	v_cndmask_b32_e64 v168, 0, 1, s[98:99]
	s_nop 0
	v_addc_co_u32_e32 v167, vcc, v167, v168, vcc
	s_waitcnt lgkmcnt(0)
	v_cmp_gt_f32_e64 s[16:17], v172, v185
	v_cmp_gt_f32_e32 vcc, v173, v185
	s_nop 0
	v_cndmask_b32_e64 v168, 0, 1, s[16:17]
	v_addc_co_u32_e32 v167, vcc, v167, v168, vcc
	ds_read_b128 v[168:171], v154 offset:128
	v_cmp_gt_f32_e64 s[16:17], v174, v185
	v_cmp_gt_f32_e32 vcc, v175, v185
	s_nop 0
	v_cndmask_b32_e64 v172, 0, 1, s[16:17]
	v_addc_co_u32_e32 v167, vcc, v167, v172, vcc
	ds_read_b128 v[172:175], v154 offset:144
	s_waitcnt lgkmcnt(1)
	v_cmp_gt_f32_e64 s[16:17], v168, v185
	v_cmp_gt_f32_e32 vcc, v169, v185
	v_cmp_gt_f32_e64 s[98:99], v170, v185
	v_cndmask_b32_e64 v168, 0, 1, s[16:17]
	v_addc_co_u32_e32 v167, vcc, v167, v168, vcc
	v_cmp_gt_f32_e32 vcc, v171, v185
	v_cndmask_b32_e64 v168, 0, 1, s[98:99]
	s_nop 0
	v_addc_co_u32_e32 v167, vcc, v167, v168, vcc
	s_waitcnt lgkmcnt(0)
	v_cmp_gt_f32_e64 s[16:17], v172, v185
	v_cmp_gt_f32_e32 vcc, v173, v185
	s_nop 0
	v_cndmask_b32_e64 v168, 0, 1, s[16:17]
	v_addc_co_u32_e32 v167, vcc, v167, v168, vcc
	ds_read_b128 v[168:171], v154 offset:160
	v_cmp_gt_f32_e64 s[16:17], v174, v185
	v_cmp_gt_f32_e32 vcc, v175, v185
	s_nop 0
	v_cndmask_b32_e64 v172, 0, 1, s[16:17]
	v_addc_co_u32_e32 v167, vcc, v167, v172, vcc
	ds_read_b128 v[172:175], v154 offset:176
	s_waitcnt lgkmcnt(1)
	v_cmp_gt_f32_e64 s[16:17], v168, v185
	v_cmp_gt_f32_e32 vcc, v169, v185
	v_cmp_gt_f32_e64 s[98:99], v170, v185
	v_cndmask_b32_e64 v168, 0, 1, s[16:17]
	v_addc_co_u32_e32 v167, vcc, v167, v168, vcc
	v_cmp_gt_f32_e32 vcc, v171, v185
	v_cndmask_b32_e64 v168, 0, 1, s[98:99]
	s_nop 0
	v_addc_co_u32_e32 v167, vcc, v167, v168, vcc
	s_waitcnt lgkmcnt(0)
	v_cmp_gt_f32_e64 s[16:17], v172, v185
	v_cmp_gt_f32_e32 vcc, v173, v185
	s_nop 0
	v_cndmask_b32_e64 v168, 0, 1, s[16:17]
	v_addc_co_u32_e32 v167, vcc, v167, v168, vcc
	ds_read_b128 v[168:171], v154 offset:192
	v_cmp_gt_f32_e64 s[16:17], v174, v185
	v_cmp_gt_f32_e32 vcc, v175, v185
	s_nop 0
	v_cndmask_b32_e64 v172, 0, 1, s[16:17]
	v_addc_co_u32_e32 v167, vcc, v167, v172, vcc
	ds_read_b128 v[172:175], v154 offset:256
	s_waitcnt lgkmcnt(1)
	v_cmp_gt_f32_e32 vcc, v168, v185
	s_nop 1
	v_cndmask_b32_e64 v168, 0, 1, vcc
	v_cmp_gt_f32_e32 vcc, v169, v185
	v_and_b32_e32 v169, 0x7f, v187
	v_bitop3_b32 v156, v169, s9, v156 bitop3:0x36
	v_addc_co_u32_e32 v167, vcc, v167, v168, vcc
	s_nop 0
	s_nop 0
	s_nop 0
	s_nop 0
	s_nop 0
	v_cmp_gt_u32_e32 vcc, 16, v167
	s_and_b64 vcc, s[4:5], vcc
	s_nop 0
	v_cndmask_b32_e32 v167, v150, v167, vcc
	v_lshlrev_b32_e32 v167, 2, v167
	ds_permute_b32 v168, v167, v185
	s_waitcnt lgkmcnt(1)
	v_cmp_gt_f32_e32 vcc, v173, v186
	ds_permute_b32 v176, v167, v184
	s_waitcnt lgkmcnt(1)
	v_cndmask_b32_e64 v177, 0, v168, s[44:45]
	v_cndmask_b32_e64 v167, 0, 1, vcc
	v_cmp_gt_f32_e32 vcc, v172, v186
	ds_read_b128 v[168:171], v154 offset:272
	s_nop 0
	v_addc_co_u32_e32 v167, vcc, 0, v167, vcc
	v_cmp_gt_f32_e64 s[16:17], v174, v186
	v_cmp_gt_f32_e32 vcc, v175, v186
	s_nop 0
	v_cndmask_b32_e64 v172, 0, 1, s[16:17]
	v_addc_co_u32_e32 v167, vcc, v167, v172, vcc
	ds_read_b128 v[172:175], v154 offset:288
	s_waitcnt lgkmcnt(1)
	v_cmp_gt_f32_e64 s[16:17], v168, v186
	v_cmp_gt_f32_e32 vcc, v169, v186
	v_cmp_gt_f32_e64 s[98:99], v170, v186
	v_cndmask_b32_e64 v168, 0, 1, s[16:17]
	v_addc_co_u32_e32 v167, vcc, v167, v168, vcc
	v_cmp_gt_f32_e32 vcc, v171, v186
	v_cndmask_b32_e64 v168, 0, 1, s[98:99]
	s_nop 0
	v_addc_co_u32_e32 v167, vcc, v167, v168, vcc
	s_waitcnt lgkmcnt(0)
	v_cmp_gt_f32_e64 s[16:17], v172, v186
	v_cmp_gt_f32_e32 vcc, v173, v186
	s_nop 0
	v_cndmask_b32_e64 v168, 0, 1, s[16:17]
	v_addc_co_u32_e32 v167, vcc, v167, v168, vcc
	ds_read_b128 v[168:171], v154 offset:304
	v_cmp_gt_f32_e64 s[16:17], v174, v186
	v_cmp_gt_f32_e32 vcc, v175, v186
	s_nop 0
	v_cndmask_b32_e64 v172, 0, 1, s[16:17]
	v_addc_co_u32_e32 v167, vcc, v167, v172, vcc
	ds_read_b128 v[172:175], v154 offset:320
	s_waitcnt lgkmcnt(1)
	v_cmp_gt_f32_e64 s[16:17], v168, v186
	v_cmp_gt_f32_e32 vcc, v169, v186
	v_cmp_gt_f32_e64 s[98:99], v170, v186
	v_cndmask_b32_e64 v168, 0, 1, s[16:17]
	v_addc_co_u32_e32 v167, vcc, v167, v168, vcc
	v_cmp_gt_f32_e32 vcc, v171, v186
	v_cndmask_b32_e64 v168, 0, 1, s[98:99]
	s_nop 0
	v_addc_co_u32_e32 v167, vcc, v167, v168, vcc
	s_waitcnt lgkmcnt(0)
	v_cmp_gt_f32_e64 s[16:17], v172, v186
	v_cmp_gt_f32_e32 vcc, v173, v186
	s_nop 0
	v_cndmask_b32_e64 v168, 0, 1, s[16:17]
	v_addc_co_u32_e32 v167, vcc, v167, v168, vcc
	ds_read_b128 v[168:171], v154 offset:336
	v_cmp_gt_f32_e64 s[16:17], v174, v186
	v_cmp_gt_f32_e32 vcc, v175, v186
	s_nop 0
	v_cndmask_b32_e64 v172, 0, 1, s[16:17]
	v_addc_co_u32_e32 v167, vcc, v167, v172, vcc
	ds_read_b128 v[172:175], v154 offset:352
	s_waitcnt lgkmcnt(1)
	v_cmp_gt_f32_e64 s[16:17], v168, v186
	v_cmp_gt_f32_e32 vcc, v169, v186
	v_cmp_gt_f32_e64 s[98:99], v170, v186
	v_cndmask_b32_e64 v168, 0, 1, s[16:17]
	v_addc_co_u32_e32 v167, vcc, v167, v168, vcc
	v_cmp_gt_f32_e32 vcc, v171, v186
	v_cndmask_b32_e64 v168, 0, 1, s[98:99]
	s_nop 0
	v_addc_co_u32_e32 v167, vcc, v167, v168, vcc
	s_waitcnt lgkmcnt(0)
	v_cmp_gt_f32_e64 s[16:17], v172, v186
	v_cmp_gt_f32_e32 vcc, v173, v186
	s_nop 0
	v_cndmask_b32_e64 v168, 0, 1, s[16:17]
	v_addc_co_u32_e32 v167, vcc, v167, v168, vcc
	ds_read_b128 v[168:171], v154 offset:368
	v_cmp_gt_f32_e64 s[16:17], v174, v186
	v_cmp_gt_f32_e32 vcc, v175, v186
	s_nop 0
	v_cndmask_b32_e64 v172, 0, 1, s[16:17]
	v_addc_co_u32_e32 v167, vcc, v167, v172, vcc
	ds_read_b128 v[172:175], v154 offset:384
	s_waitcnt lgkmcnt(1)
	v_cmp_gt_f32_e64 s[16:17], v168, v186
	v_cmp_gt_f32_e32 vcc, v169, v186
	v_cmp_gt_f32_e64 s[98:99], v170, v186
	v_cndmask_b32_e64 v168, 0, 1, s[16:17]
	v_addc_co_u32_e32 v167, vcc, v167, v168, vcc
	v_cmp_gt_f32_e32 vcc, v171, v186
	v_cndmask_b32_e64 v168, 0, 1, s[98:99]
	s_nop 0
	v_addc_co_u32_e32 v167, vcc, v167, v168, vcc
	s_waitcnt lgkmcnt(0)
	v_cmp_gt_f32_e64 s[16:17], v172, v186
	v_cmp_gt_f32_e32 vcc, v173, v186
	s_nop 0
	v_cndmask_b32_e64 v168, 0, 1, s[16:17]
	v_addc_co_u32_e32 v167, vcc, v167, v168, vcc
	ds_read_b128 v[168:171], v154 offset:400
	v_cmp_gt_f32_e64 s[16:17], v174, v186
	v_cmp_gt_f32_e32 vcc, v175, v186
	s_nop 0
	v_cndmask_b32_e64 v172, 0, 1, s[16:17]
	v_addc_co_u32_e32 v167, vcc, v167, v172, vcc
	ds_read_b128 v[172:175], v154 offset:416
	s_waitcnt lgkmcnt(1)
	v_cmp_gt_f32_e64 s[16:17], v168, v186
	v_cmp_gt_f32_e32 vcc, v169, v186
	v_cmp_gt_f32_e64 s[98:99], v170, v186
	v_cndmask_b32_e64 v168, 0, 1, s[16:17]
	v_addc_co_u32_e32 v167, vcc, v167, v168, vcc
	v_cmp_gt_f32_e32 vcc, v171, v186
	v_cndmask_b32_e64 v168, 0, 1, s[98:99]
	s_nop 0
	v_addc_co_u32_e32 v167, vcc, v167, v168, vcc
	s_waitcnt lgkmcnt(0)
	v_cmp_gt_f32_e64 s[16:17], v172, v186
	v_cmp_gt_f32_e32 vcc, v173, v186
	s_nop 0
	v_cndmask_b32_e64 v168, 0, 1, s[16:17]
	v_addc_co_u32_e32 v167, vcc, v167, v168, vcc
	ds_read_b128 v[168:171], v154 offset:432
	v_cmp_gt_f32_e64 s[16:17], v174, v186
	v_cmp_gt_f32_e32 vcc, v175, v186
	s_nop 0
	v_cndmask_b32_e64 v172, 0, 1, s[16:17]
	v_addc_co_u32_e32 v167, vcc, v167, v172, vcc
	ds_read_b128 v[172:175], v154 offset:448
	s_waitcnt lgkmcnt(1)
	v_cmp_gt_f32_e64 s[16:17], v168, v186
	v_cmp_gt_f32_e32 vcc, v169, v186
	v_cmp_gt_f32_e64 s[98:99], v170, v186
	v_cndmask_b32_e64 v168, 0, 1, s[16:17]
	v_addc_co_u32_e32 v167, vcc, v167, v168, vcc
	v_cmp_gt_f32_e32 vcc, v171, v186
	v_cndmask_b32_e64 v168, 0, 1, s[98:99]
	s_nop 0
	v_addc_co_u32_e32 v167, vcc, v167, v168, vcc
	s_waitcnt lgkmcnt(0)
	v_cmp_gt_f32_e64 s[16:17], v172, v186
	v_cmp_gt_f32_e32 vcc, v173, v186
	s_nop 0
	v_cndmask_b32_e64 v168, 0, 1, s[16:17]
	v_addc_co_u32_e32 v167, vcc, v167, v168, vcc
	s_nop 0
	s_nop 1
	s_nop 0
	s_nop 0
	ds_read_b128 v[172:175], v154 offset:528
	s_nop 0
	s_nop 0
	ds_read_b128 v[168:171], v154 offset:512
	v_cmp_gt_u32_e32 vcc, 16, v167
	v_add_u32_e32 v167, 16, v167
	s_and_b64 vcc, s[4:5], vcc
	v_cndmask_b32_e32 v167, v151, v167, vcc
	v_lshlrev_b32_e32 v167, 2, v167
	s_waitcnt lgkmcnt(0)
	v_cmp_gt_f32_e32 vcc, v169, v165
	ds_permute_b32 v179, v167, v166
	ds_permute_b32 v178, v167, v186
	v_cndmask_b32_e64 v166, 0, 1, vcc
	v_cmp_gt_f32_e32 vcc, v168, v165
	s_nop 1
	v_addc_co_u32_e32 v166, vcc, 0, v166, vcc
	v_cmp_gt_f32_e64 s[16:17], v170, v165
	v_cmp_gt_f32_e32 vcc, v171, v165
	v_cmp_gt_f32_e64 s[98:99], v172, v165
	v_cndmask_b32_e64 v167, 0, 1, s[16:17]
	v_addc_co_u32_e32 v166, vcc, v166, v167, vcc
	v_cmp_gt_f32_e32 vcc, v173, v165
	v_cndmask_b32_e64 v167, 0, 1, s[98:99]
	s_nop 0
	v_addc_co_u32_e32 v170, vcc, v166, v167, vcc
	ds_read_b128 v[166:169], v154 offset:544
	v_cmp_gt_f32_e64 s[16:17], v174, v165
	v_cmp_gt_f32_e32 vcc, v175, v165
	s_nop 0
	v_cndmask_b32_e64 v171, 0, 1, s[16:17]
	v_addc_co_u32_e32 v174, vcc, v170, v171, vcc
	ds_read_b128 v[170:173], v154 offset:560
	s_waitcnt lgkmcnt(1)
	v_cmp_gt_f32_e64 s[16:17], v166, v165
	v_cmp_gt_f32_e32 vcc, v167, v165
	v_cmp_gt_f32_e64 s[98:99], v168, v165
	v_cndmask_b32_e64 v166, 0, 1, s[16:17]
	v_addc_co_u32_e32 v166, vcc, v174, v166, vcc
	v_cmp_gt_f32_e32 vcc, v169, v165
	v_cndmask_b32_e64 v167, 0, 1, s[98:99]
	s_nop 0
	v_addc_co_u32_e32 v166, vcc, v166, v167, vcc
	s_waitcnt lgkmcnt(0)
	v_cmp_gt_f32_e64 s[16:17], v170, v165
	v_cmp_gt_f32_e32 vcc, v171, v165
	s_nop 0
	v_cndmask_b32_e64 v167, 0, 1, s[16:17]
	v_addc_co_u32_e32 v170, vcc, v166, v167, vcc
	ds_read_b128 v[166:169], v154 offset:576
	v_cmp_gt_f32_e64 s[16:17], v172, v165
	v_cmp_gt_f32_e32 vcc, v173, v165
	s_nop 0
	v_cndmask_b32_e64 v171, 0, 1, s[16:17]
	v_addc_co_u32_e32 v174, vcc, v170, v171, vcc
	ds_read_b128 v[170:173], v154 offset:592
	s_waitcnt lgkmcnt(1)
	v_cmp_gt_f32_e64 s[16:17], v166, v165
	v_cmp_gt_f32_e32 vcc, v167, v165
	v_cmp_gt_f32_e64 s[98:99], v168, v165
	v_cndmask_b32_e64 v166, 0, 1, s[16:17]
	v_addc_co_u32_e32 v166, vcc, v174, v166, vcc
	v_cmp_gt_f32_e32 vcc, v169, v165
	v_cndmask_b32_e64 v167, 0, 1, s[98:99]
	s_nop 0
	v_addc_co_u32_e32 v166, vcc, v166, v167, vcc
	s_waitcnt lgkmcnt(0)
	v_cmp_gt_f32_e64 s[16:17], v170, v165
	v_cmp_gt_f32_e32 vcc, v171, v165
	s_nop 0
	v_cndmask_b32_e64 v167, 0, 1, s[16:17]
	v_addc_co_u32_e32 v170, vcc, v166, v167, vcc
	ds_read_b128 v[166:169], v154 offset:608
	v_cmp_gt_f32_e64 s[16:17], v172, v165
	v_cmp_gt_f32_e32 vcc, v173, v165
	s_nop 0
	v_cndmask_b32_e64 v171, 0, 1, s[16:17]
	v_addc_co_u32_e32 v174, vcc, v170, v171, vcc
	ds_read_b128 v[170:173], v154 offset:624
	s_waitcnt lgkmcnt(1)
	v_cmp_gt_f32_e64 s[16:17], v166, v165
	v_cmp_gt_f32_e32 vcc, v167, v165
	v_cmp_gt_f32_e64 s[98:99], v168, v165
	v_cndmask_b32_e64 v166, 0, 1, s[16:17]
	v_addc_co_u32_e32 v166, vcc, v174, v166, vcc
	v_cmp_gt_f32_e32 vcc, v169, v165
	v_cndmask_b32_e64 v167, 0, 1, s[98:99]
	s_nop 0
	v_addc_co_u32_e32 v166, vcc, v166, v167, vcc
	s_waitcnt lgkmcnt(0)
	v_cmp_gt_f32_e64 s[16:17], v170, v165
	v_cmp_gt_f32_e32 vcc, v171, v165
	s_nop 0
	v_cndmask_b32_e64 v167, 0, 1, s[16:17]
	v_addc_co_u32_e32 v170, vcc, v166, v167, vcc
	ds_read_b128 v[166:169], v154 offset:640
	v_cmp_gt_f32_e64 s[16:17], v172, v165
	v_cmp_gt_f32_e32 vcc, v173, v165
	s_nop 0
	v_cndmask_b32_e64 v171, 0, 1, s[16:17]
	v_addc_co_u32_e32 v174, vcc, v170, v171, vcc
	ds_read_b128 v[170:173], v154 offset:656
	s_waitcnt lgkmcnt(1)
	v_cmp_gt_f32_e64 s[16:17], v166, v165
	v_cmp_gt_f32_e32 vcc, v167, v165
	v_cmp_gt_f32_e64 s[98:99], v168, v165
	v_cndmask_b32_e64 v166, 0, 1, s[16:17]
	v_addc_co_u32_e32 v166, vcc, v174, v166, vcc
	v_cmp_gt_f32_e32 vcc, v169, v165
	v_cndmask_b32_e64 v167, 0, 1, s[98:99]
	s_nop 0
	v_addc_co_u32_e32 v166, vcc, v166, v167, vcc
	s_waitcnt lgkmcnt(0)
	v_cmp_gt_f32_e64 s[16:17], v170, v165
	v_cmp_gt_f32_e32 vcc, v171, v165
	s_nop 0
	v_cndmask_b32_e64 v167, 0, 1, s[16:17]
	v_addc_co_u32_e32 v170, vcc, v166, v167, vcc
	ds_read_b128 v[166:169], v154 offset:672
	v_cmp_gt_f32_e64 s[16:17], v172, v165
	v_cmp_gt_f32_e32 vcc, v173, v165
	s_nop 0
	v_cndmask_b32_e64 v171, 0, 1, s[16:17]
	v_addc_co_u32_e32 v174, vcc, v170, v171, vcc
	ds_read_b128 v[170:173], v154 offset:688
	s_waitcnt lgkmcnt(1)
	v_cmp_gt_f32_e64 s[16:17], v166, v165
	v_cmp_gt_f32_e32 vcc, v167, v165
	v_cmp_gt_f32_e64 s[98:99], v168, v165
	v_cndmask_b32_e64 v166, 0, 1, s[16:17]
	v_addc_co_u32_e32 v166, vcc, v174, v166, vcc
	v_cmp_gt_f32_e32 vcc, v169, v165
	v_cndmask_b32_e64 v167, 0, 1, s[98:99]
	s_nop 0
	v_addc_co_u32_e32 v166, vcc, v166, v167, vcc
	s_waitcnt lgkmcnt(0)
	v_cmp_gt_f32_e64 s[16:17], v170, v165
	v_cmp_gt_f32_e32 vcc, v171, v165
	s_nop 0
	v_cndmask_b32_e64 v167, 0, 1, s[16:17]
	v_addc_co_u32_e32 v170, vcc, v166, v167, vcc
	ds_read_b128 v[166:169], v154 offset:704
	v_cmp_gt_f32_e64 s[16:17], v172, v165
	v_cmp_gt_f32_e32 vcc, v173, v165
	s_nop 0
	v_cndmask_b32_e64 v171, 0, 1, s[16:17]
	v_addc_co_u32_e32 v174, vcc, v170, v171, vcc
	ds_read_b128 v[170:173], v154 offset:768
	s_waitcnt lgkmcnt(1)
	v_cmp_gt_f32_e64 s[16:17], v166, v165
	v_cmp_gt_f32_e32 vcc, v167, v165
	s_nop 0
	v_cndmask_b32_e64 v166, 0, 1, s[16:17]
	v_addc_co_u32_e32 v166, vcc, v174, v166, vcc
	s_nop 0
	v_cndmask_b32_e64 v168, v177, v178, s[46:47]
	s_nop 0
	s_nop 0
	s_nop 0
	s_nop 1
	s_nop 0
	v_cmp_gt_u32_e32 vcc, 16, v166
	v_add_u32_e32 v166, 32, v166
	s_and_b64 vcc, s[4:5], vcc
	v_cndmask_b32_e32 v166, v152, v166, vcc
	v_lshlrev_b32_e32 v166, 2, v166
	ds_permute_b32 v165, v166, v165
	s_waitcnt lgkmcnt(1)
	v_cmp_gt_f32_e32 vcc, v171, v163
	v_cndmask_b32_e64 v167, 0, v176, s[44:45]
	ds_permute_b32 v175, v166, v164
	v_cndmask_b32_e64 v164, 0, 1, vcc
	v_cmp_gt_f32_e32 vcc, v170, v163
	v_cndmask_b32_e64 v174, v167, v179, s[46:47]
	s_waitcnt lgkmcnt(1)
	v_cndmask_b32_e64 v176, v168, v165, s[48:49]
	v_addc_co_u32_e32 v168, vcc, 0, v164, vcc
	ds_read_b128 v[164:167], v154 offset:784
	v_cmp_gt_f32_e64 s[16:17], v172, v163
	v_cmp_gt_f32_e32 vcc, v173, v163
	s_nop 0
	v_cndmask_b32_e64 v169, 0, 1, s[16:17]
	v_addc_co_u32_e32 v172, vcc, v168, v169, vcc
	ds_read_b128 v[168:171], v154 offset:800
	s_waitcnt lgkmcnt(1)
	v_cmp_gt_f32_e64 s[16:17], v164, v163
	v_cmp_gt_f32_e32 vcc, v165, v163
	v_cmp_gt_f32_e64 s[98:99], v166, v163
	v_cndmask_b32_e64 v164, 0, 1, s[16:17]
	v_addc_co_u32_e32 v164, vcc, v172, v164, vcc
	v_cmp_gt_f32_e32 vcc, v167, v163
	v_cndmask_b32_e64 v165, 0, 1, s[98:99]
	s_nop 0
	v_addc_co_u32_e32 v164, vcc, v164, v165, vcc
	s_waitcnt lgkmcnt(0)
	v_cmp_gt_f32_e64 s[16:17], v168, v163
	v_cmp_gt_f32_e32 vcc, v169, v163
	s_nop 0
	v_cndmask_b32_e64 v165, 0, 1, s[16:17]
	v_addc_co_u32_e32 v168, vcc, v164, v165, vcc
	ds_read_b128 v[164:167], v154 offset:816
	v_cmp_gt_f32_e64 s[16:17], v170, v163
	v_cmp_gt_f32_e32 vcc, v171, v163
	s_nop 0
	v_cndmask_b32_e64 v169, 0, 1, s[16:17]
	v_addc_co_u32_e32 v172, vcc, v168, v169, vcc
	ds_read_b128 v[168:171], v154 offset:832
	s_waitcnt lgkmcnt(1)
	v_cmp_gt_f32_e64 s[16:17], v164, v163
	v_cmp_gt_f32_e32 vcc, v165, v163
	v_cmp_gt_f32_e64 s[98:99], v166, v163
	v_cndmask_b32_e64 v164, 0, 1, s[16:17]
	v_addc_co_u32_e32 v164, vcc, v172, v164, vcc
	v_cmp_gt_f32_e32 vcc, v167, v163
	v_cndmask_b32_e64 v165, 0, 1, s[98:99]
	s_nop 0
	v_addc_co_u32_e32 v164, vcc, v164, v165, vcc
	s_waitcnt lgkmcnt(0)
	v_cmp_gt_f32_e64 s[16:17], v168, v163
	v_cmp_gt_f32_e32 vcc, v169, v163
	s_nop 0
	v_cndmask_b32_e64 v165, 0, 1, s[16:17]
	v_addc_co_u32_e32 v168, vcc, v164, v165, vcc
	ds_read_b128 v[164:167], v154 offset:848
	v_cmp_gt_f32_e64 s[16:17], v170, v163
	v_cmp_gt_f32_e32 vcc, v171, v163
	s_nop 0
	v_cndmask_b32_e64 v169, 0, 1, s[16:17]
	v_addc_co_u32_e32 v172, vcc, v168, v169, vcc
	ds_read_b128 v[168:171], v154 offset:864
	s_waitcnt lgkmcnt(1)
	v_cmp_gt_f32_e64 s[16:17], v164, v163
	v_cmp_gt_f32_e32 vcc, v165, v163
	v_cmp_gt_f32_e64 s[98:99], v166, v163
	v_cndmask_b32_e64 v164, 0, 1, s[16:17]
	v_addc_co_u32_e32 v164, vcc, v172, v164, vcc
	v_cmp_gt_f32_e32 vcc, v167, v163
	v_cndmask_b32_e64 v165, 0, 1, s[98:99]
	s_nop 0
	v_addc_co_u32_e32 v164, vcc, v164, v165, vcc
	s_waitcnt lgkmcnt(0)
	v_cmp_gt_f32_e64 s[16:17], v168, v163
	v_cmp_gt_f32_e32 vcc, v169, v163
	s_nop 0
	v_cndmask_b32_e64 v165, 0, 1, s[16:17]
	v_addc_co_u32_e32 v168, vcc, v164, v165, vcc
	ds_read_b128 v[164:167], v154 offset:880
	v_cmp_gt_f32_e64 s[16:17], v170, v163
	v_cmp_gt_f32_e32 vcc, v171, v163
	s_nop 0
	v_cndmask_b32_e64 v169, 0, 1, s[16:17]
	v_addc_co_u32_e32 v172, vcc, v168, v169, vcc
	ds_read_b128 v[168:171], v154 offset:896
	s_waitcnt lgkmcnt(1)
	v_cmp_gt_f32_e64 s[16:17], v164, v163
	v_cmp_gt_f32_e32 vcc, v165, v163
	v_cmp_gt_f32_e64 s[98:99], v166, v163
	v_cndmask_b32_e64 v164, 0, 1, s[16:17]
	v_addc_co_u32_e32 v164, vcc, v172, v164, vcc
	v_cmp_gt_f32_e32 vcc, v167, v163
	v_cndmask_b32_e64 v165, 0, 1, s[98:99]
	s_nop 0
	v_addc_co_u32_e32 v164, vcc, v164, v165, vcc
	s_waitcnt lgkmcnt(0)
	v_cmp_gt_f32_e64 s[16:17], v168, v163
	v_cmp_gt_f32_e32 vcc, v169, v163
	s_nop 0
	v_cndmask_b32_e64 v165, 0, 1, s[16:17]
	v_addc_co_u32_e32 v168, vcc, v164, v165, vcc
	ds_read_b128 v[164:167], v154 offset:912
	v_cmp_gt_f32_e64 s[16:17], v170, v163
	v_cmp_gt_f32_e32 vcc, v171, v163
	s_nop 0
	v_cndmask_b32_e64 v169, 0, 1, s[16:17]
	v_addc_co_u32_e32 v172, vcc, v168, v169, vcc
	ds_read_b128 v[168:171], v154 offset:928
	s_waitcnt lgkmcnt(1)
	v_cmp_gt_f32_e64 s[16:17], v164, v163
	v_cmp_gt_f32_e32 vcc, v165, v163
	v_cmp_gt_f32_e64 s[98:99], v166, v163
	v_cndmask_b32_e64 v164, 0, 1, s[16:17]
	v_addc_co_u32_e32 v164, vcc, v172, v164, vcc
	v_cmp_gt_f32_e32 vcc, v167, v163
	v_cndmask_b32_e64 v165, 0, 1, s[98:99]
	s_nop 0
	v_addc_co_u32_e32 v164, vcc, v164, v165, vcc
	s_waitcnt lgkmcnt(0)
	v_cmp_gt_f32_e64 s[16:17], v168, v163
	v_cmp_gt_f32_e32 vcc, v169, v163
	s_nop 0
	v_cndmask_b32_e64 v165, 0, 1, s[16:17]
	v_addc_co_u32_e32 v168, vcc, v164, v165, vcc
	ds_read_b128 v[164:167], v154 offset:944
	v_cmp_gt_f32_e64 s[16:17], v170, v163
	v_cmp_gt_f32_e32 vcc, v171, v163
	s_nop 0
	v_cndmask_b32_e64 v169, 0, 1, s[16:17]
	v_addc_co_u32_e32 v172, vcc, v168, v169, vcc
	ds_read_b128 v[168:171], v154 offset:960
	s_waitcnt lgkmcnt(1)
	v_cmp_gt_f32_e64 s[16:17], v164, v163
	v_cmp_gt_f32_e32 vcc, v165, v163
	v_cmp_gt_f32_e64 s[98:99], v166, v163
	v_cndmask_b32_e64 v164, 0, 1, s[16:17]
	v_addc_co_u32_e32 v164, vcc, v172, v164, vcc
	v_cmp_gt_f32_e32 vcc, v167, v163
	v_cndmask_b32_e64 v165, 0, 1, s[98:99]
	s_nop 0
	v_addc_co_u32_e32 v164, vcc, v164, v165, vcc
	s_waitcnt lgkmcnt(0)
	v_cmp_gt_f32_e64 s[16:17], v168, v163
	v_cmp_gt_f32_e32 vcc, v169, v163
	s_nop 0
	v_cndmask_b32_e64 v165, 0, 1, s[16:17]
	v_addc_co_u32_e32 v164, vcc, v164, v165, vcc
	s_nop 0
	s_nop 0
	s_nop 0
	s_nop 0
	v_cmp_gt_u32_e32 vcc, 16, v164
	v_add_u32_e32 v164, 48, v164
	s_and_b64 vcc, s[4:5], vcc
	v_cndmask_b32_e32 v168, v140, v164, vcc
	ds_read_b128 v[164:167], v154 offset:1024
	v_lshlrev_b32_e32 v168, 2, v168
	ds_permute_b32 v172, v168, v163
	ds_permute_b32 v173, v168, v162
	ds_read_b128 v[168:171], v154 offset:1040
	s_waitcnt lgkmcnt(3)
	v_cmp_gt_f32_e64 s[16:17], v165, v161
	v_cmp_gt_f32_e32 vcc, v164, v161
	v_cmp_gt_f32_e64 s[98:99], v166, v161
	v_cndmask_b32_e64 v162, 0, 1, s[16:17]
	v_addc_co_u32_e32 v162, vcc, 0, v162, vcc
	v_cmp_gt_f32_e32 vcc, v167, v161
	v_cndmask_b32_e64 v163, 0, 1, s[98:99]
	s_nop 0
	v_addc_co_u32_e32 v162, vcc, v162, v163, vcc
	s_waitcnt lgkmcnt(0)
	v_cmp_gt_f32_e64 s[16:17], v168, v161
	v_cmp_gt_f32_e32 vcc, v169, v161
	s_nop 0
	v_cndmask_b32_e64 v163, 0, 1, s[16:17]
	v_addc_co_u32_e32 v166, vcc, v162, v163, vcc
	ds_read_b128 v[162:165], v154 offset:1056
	v_cmp_gt_f32_e64 s[16:17], v170, v161
	v_cmp_gt_f32_e32 vcc, v171, v161
	s_nop 0
	v_cndmask_b32_e64 v167, 0, 1, s[16:17]
	v_addc_co_u32_e32 v170, vcc, v166, v167, vcc
	ds_read_b128 v[166:169], v154 offset:1072
	s_waitcnt lgkmcnt(1)
	v_cmp_gt_f32_e64 s[16:17], v162, v161
	v_cmp_gt_f32_e32 vcc, v163, v161
	v_cmp_gt_f32_e64 s[98:99], v164, v161
	v_cndmask_b32_e64 v162, 0, 1, s[16:17]
	v_addc_co_u32_e32 v162, vcc, v170, v162, vcc
	v_cmp_gt_f32_e32 vcc, v165, v161
	v_cndmask_b32_e64 v163, 0, 1, s[98:99]
	s_nop 0
	v_addc_co_u32_e32 v162, vcc, v162, v163, vcc
	s_waitcnt lgkmcnt(0)
	v_cmp_gt_f32_e64 s[16:17], v166, v161
	v_cmp_gt_f32_e32 vcc, v167, v161
	s_nop 0
	v_cndmask_b32_e64 v163, 0, 1, s[16:17]
	v_addc_co_u32_e32 v166, vcc, v162, v163, vcc
	ds_read_b128 v[162:165], v154 offset:1088
	v_cmp_gt_f32_e64 s[16:17], v168, v161
	v_cmp_gt_f32_e32 vcc, v169, v161
	s_nop 0
	v_cndmask_b32_e64 v167, 0, 1, s[16:17]
	v_addc_co_u32_e32 v170, vcc, v166, v167, vcc
	ds_read_b128 v[166:169], v154 offset:1104
	s_waitcnt lgkmcnt(1)
	v_cmp_gt_f32_e64 s[16:17], v162, v161
	v_cmp_gt_f32_e32 vcc, v163, v161
	v_cmp_gt_f32_e64 s[98:99], v164, v161
	v_cndmask_b32_e64 v162, 0, 1, s[16:17]
	v_addc_co_u32_e32 v162, vcc, v170, v162, vcc
	v_cmp_gt_f32_e32 vcc, v165, v161
	v_cndmask_b32_e64 v163, 0, 1, s[98:99]
	s_nop 0
	v_addc_co_u32_e32 v162, vcc, v162, v163, vcc
	s_waitcnt lgkmcnt(0)
	v_cmp_gt_f32_e64 s[16:17], v166, v161
	v_cmp_gt_f32_e32 vcc, v167, v161
	s_nop 0
	v_cndmask_b32_e64 v163, 0, 1, s[16:17]
	v_addc_co_u32_e32 v166, vcc, v162, v163, vcc
	ds_read_b128 v[162:165], v154 offset:1120
	v_cmp_gt_f32_e64 s[16:17], v168, v161
	v_cmp_gt_f32_e32 vcc, v169, v161
	s_nop 0
	v_cndmask_b32_e64 v167, 0, 1, s[16:17]
	v_addc_co_u32_e32 v170, vcc, v166, v167, vcc
	ds_read_b128 v[166:169], v154 offset:1136
	s_waitcnt lgkmcnt(1)
	v_cmp_gt_f32_e64 s[16:17], v162, v161
	v_cmp_gt_f32_e32 vcc, v163, v161
	v_cmp_gt_f32_e64 s[98:99], v164, v161
	v_cndmask_b32_e64 v162, 0, 1, s[16:17]
	v_addc_co_u32_e32 v162, vcc, v170, v162, vcc
	v_cmp_gt_f32_e32 vcc, v165, v161
	v_cndmask_b32_e64 v163, 0, 1, s[98:99]
	s_nop 0
	v_addc_co_u32_e32 v162, vcc, v162, v163, vcc
	s_waitcnt lgkmcnt(0)
	v_cmp_gt_f32_e64 s[16:17], v166, v161
	v_cmp_gt_f32_e32 vcc, v167, v161
	s_nop 0
	v_cndmask_b32_e64 v163, 0, 1, s[16:17]
	v_addc_co_u32_e32 v166, vcc, v162, v163, vcc
	ds_read_b128 v[162:165], v154 offset:1152
	v_cmp_gt_f32_e64 s[16:17], v168, v161
	v_cmp_gt_f32_e32 vcc, v169, v161
	s_nop 0
	v_cndmask_b32_e64 v167, 0, 1, s[16:17]
	v_addc_co_u32_e32 v170, vcc, v166, v167, vcc
	ds_read_b128 v[166:169], v154 offset:1168
	s_waitcnt lgkmcnt(1)
	v_cmp_gt_f32_e64 s[16:17], v162, v161
	v_cmp_gt_f32_e32 vcc, v163, v161
	v_cmp_gt_f32_e64 s[98:99], v164, v161
	v_cndmask_b32_e64 v162, 0, 1, s[16:17]
	v_addc_co_u32_e32 v162, vcc, v170, v162, vcc
	v_cmp_gt_f32_e32 vcc, v165, v161
	v_cndmask_b32_e64 v163, 0, 1, s[98:99]
	s_nop 0
	v_addc_co_u32_e32 v162, vcc, v162, v163, vcc
	s_waitcnt lgkmcnt(0)
	v_cmp_gt_f32_e64 s[16:17], v166, v161
	v_cmp_gt_f32_e32 vcc, v167, v161
	s_nop 0
	v_cndmask_b32_e64 v163, 0, 1, s[16:17]
	v_addc_co_u32_e32 v166, vcc, v162, v163, vcc
	ds_read_b128 v[162:165], v154 offset:1184
	v_cmp_gt_f32_e64 s[16:17], v168, v161
	v_cmp_gt_f32_e32 vcc, v169, v161
	s_nop 0
	v_cndmask_b32_e64 v167, 0, 1, s[16:17]
	v_addc_co_u32_e32 v170, vcc, v166, v167, vcc
	ds_read_b128 v[166:169], v154 offset:1200
	s_waitcnt lgkmcnt(1)
	v_cmp_gt_f32_e64 s[16:17], v162, v161
	v_cmp_gt_f32_e32 vcc, v163, v161
	v_cmp_gt_f32_e64 s[98:99], v164, v161
	v_cndmask_b32_e64 v162, 0, 1, s[16:17]
	v_addc_co_u32_e32 v162, vcc, v170, v162, vcc
	v_cmp_gt_f32_e32 vcc, v165, v161
	v_cndmask_b32_e64 v163, 0, 1, s[98:99]
	s_nop 0
	v_addc_co_u32_e32 v162, vcc, v162, v163, vcc
	s_waitcnt lgkmcnt(0)
	v_cmp_gt_f32_e64 s[16:17], v166, v161
	v_cmp_gt_f32_e32 vcc, v167, v161
	s_nop 0
	v_cndmask_b32_e64 v163, 0, 1, s[16:17]
	v_addc_co_u32_e32 v166, vcc, v162, v163, vcc
	ds_read_b128 v[162:165], v154 offset:1216
	v_cmp_gt_f32_e64 s[16:17], v168, v161
	v_cmp_gt_f32_e32 vcc, v169, v161
	s_nop 0
	v_cndmask_b32_e64 v167, 0, 1, s[16:17]
	v_addc_co_u32_e32 v170, vcc, v166, v167, vcc
	ds_read_b128 v[166:169], v154 offset:1280
	s_waitcnt lgkmcnt(1)
	v_cmp_gt_f32_e64 s[16:17], v162, v161
	v_cmp_gt_f32_e32 vcc, v163, v161
	s_nop 0
	v_cndmask_b32_e64 v162, 0, 1, s[16:17]
	v_addc_co_u32_e32 v162, vcc, v170, v162, vcc
	s_nop 0
	s_nop 0
	s_nop 0
	s_nop 0
	v_cmp_gt_u32_e32 vcc, 16, v162
	s_and_b64 vcc, s[4:5], vcc
	s_nop 0
	v_cndmask_b32_e32 v162, v150, v162, vcc
	v_lshlrev_b32_e32 v163, 2, v162
	ds_permute_b32 v164, v163, v161
	s_waitcnt lgkmcnt(1)
	v_cmp_gt_f32_e32 vcc, v167, v159
	ds_permute_b32 v160, v163, v160
	v_cndmask_b32_e64 v162, v176, v172, s[50:51]
	v_cndmask_b32_e64 v161, v174, v175, s[48:49]
	s_waitcnt lgkmcnt(1)
	v_cndmask_b32_e64 v163, 0, v164, s[44:45]
	v_cndmask_b32_e64 v164, 0, 1, vcc
	v_cmp_gt_f32_e32 vcc, v166, v159
	s_waitcnt lgkmcnt(0)
	v_cndmask_b32_e64 v160, 0, v160, s[44:45]
	v_cndmask_b32_e64 v161, v161, v173, s[50:51]
	v_addc_co_u32_e32 v170, vcc, 0, v164, vcc
	ds_read_b128 v[164:167], v154 offset:1296
	v_cmp_gt_f32_e32 vcc, v168, v159
	v_lshlrev_b32_e32 v161, 7, v161
	s_nop 0
	v_cndmask_b32_e64 v168, 0, 1, vcc
	v_cmp_gt_f32_e32 vcc, v169, v159
	s_nop 1
	v_addc_co_u32_e32 v172, vcc, v170, v168, vcc
	ds_read_b128 v[168:171], v154 offset:1312
	s_waitcnt lgkmcnt(1)
	v_cmp_gt_f32_e64 s[16:17], v164, v159
	v_cmp_gt_f32_e32 vcc, v165, v159
	v_cmp_gt_f32_e64 s[98:99], v166, v159
	v_cndmask_b32_e64 v164, 0, 1, s[16:17]
	v_addc_co_u32_e32 v164, vcc, v172, v164, vcc
	v_cmp_gt_f32_e32 vcc, v167, v159
	v_cndmask_b32_e64 v165, 0, 1, s[98:99]
	s_nop 0
	v_addc_co_u32_e32 v164, vcc, v164, v165, vcc
	s_waitcnt lgkmcnt(0)
	v_cmp_gt_f32_e64 s[16:17], v168, v159
	v_cmp_gt_f32_e32 vcc, v169, v159
	s_nop 0
	v_cndmask_b32_e64 v165, 0, 1, s[16:17]
	v_addc_co_u32_e32 v168, vcc, v164, v165, vcc
	ds_read_b128 v[164:167], v154 offset:1328
	v_cmp_gt_f32_e64 s[16:17], v170, v159
	v_cmp_gt_f32_e32 vcc, v171, v159
	s_nop 0
	v_cndmask_b32_e64 v169, 0, 1, s[16:17]
	v_addc_co_u32_e32 v172, vcc, v168, v169, vcc
	ds_read_b128 v[168:171], v154 offset:1344
	s_waitcnt lgkmcnt(1)
	v_cmp_gt_f32_e64 s[16:17], v164, v159
	v_cmp_gt_f32_e32 vcc, v165, v159
	v_cmp_gt_f32_e64 s[98:99], v166, v159
	v_cndmask_b32_e64 v164, 0, 1, s[16:17]
	v_addc_co_u32_e32 v164, vcc, v172, v164, vcc
	v_cmp_gt_f32_e32 vcc, v167, v159
	v_cndmask_b32_e64 v165, 0, 1, s[98:99]
	s_nop 0
	v_addc_co_u32_e32 v164, vcc, v164, v165, vcc
	s_waitcnt lgkmcnt(0)
	v_cmp_gt_f32_e64 s[16:17], v168, v159
	v_cmp_gt_f32_e32 vcc, v169, v159
	s_nop 0
	v_cndmask_b32_e64 v165, 0, 1, s[16:17]
	v_addc_co_u32_e32 v168, vcc, v164, v165, vcc
	ds_read_b128 v[164:167], v154 offset:1360
	v_cmp_gt_f32_e64 s[16:17], v170, v159
	v_cmp_gt_f32_e32 vcc, v171, v159
	s_nop 0
	v_cndmask_b32_e64 v169, 0, 1, s[16:17]
	v_addc_co_u32_e32 v172, vcc, v168, v169, vcc
	ds_read_b128 v[168:171], v154 offset:1376
	s_waitcnt lgkmcnt(1)
	v_cmp_gt_f32_e64 s[16:17], v164, v159
	v_cmp_gt_f32_e32 vcc, v165, v159
	v_cmp_gt_f32_e64 s[98:99], v166, v159
	v_cndmask_b32_e64 v164, 0, 1, s[16:17]
	v_addc_co_u32_e32 v164, vcc, v172, v164, vcc
	v_cmp_gt_f32_e32 vcc, v167, v159
	v_cndmask_b32_e64 v165, 0, 1, s[98:99]
	s_nop 0
	v_addc_co_u32_e32 v164, vcc, v164, v165, vcc
	s_waitcnt lgkmcnt(0)
	v_cmp_gt_f32_e64 s[16:17], v168, v159
	v_cmp_gt_f32_e32 vcc, v169, v159
	s_nop 0
	v_cndmask_b32_e64 v165, 0, 1, s[16:17]
	v_addc_co_u32_e32 v168, vcc, v164, v165, vcc
	ds_read_b128 v[164:167], v154 offset:1392
	v_cmp_gt_f32_e64 s[16:17], v170, v159
	v_cmp_gt_f32_e32 vcc, v171, v159
	s_nop 0
	v_cndmask_b32_e64 v169, 0, 1, s[16:17]
	v_addc_co_u32_e32 v172, vcc, v168, v169, vcc
	ds_read_b128 v[168:171], v154 offset:1408
	s_waitcnt lgkmcnt(1)
	v_cmp_gt_f32_e64 s[16:17], v164, v159
	v_cmp_gt_f32_e32 vcc, v165, v159
	v_cmp_gt_f32_e64 s[98:99], v166, v159
	v_cndmask_b32_e64 v164, 0, 1, s[16:17]
	v_addc_co_u32_e32 v164, vcc, v172, v164, vcc
	v_cmp_gt_f32_e32 vcc, v167, v159
	v_cndmask_b32_e64 v165, 0, 1, s[98:99]
	s_nop 0
	v_addc_co_u32_e32 v164, vcc, v164, v165, vcc
	s_waitcnt lgkmcnt(0)
	v_cmp_gt_f32_e64 s[16:17], v168, v159
	v_cmp_gt_f32_e32 vcc, v169, v159
	s_nop 0
	v_cndmask_b32_e64 v165, 0, 1, s[16:17]
	v_addc_co_u32_e32 v168, vcc, v164, v165, vcc
	ds_read_b128 v[164:167], v154 offset:1424
	v_cmp_gt_f32_e64 s[16:17], v170, v159
	v_cmp_gt_f32_e32 vcc, v171, v159
	s_nop 0
	v_cndmask_b32_e64 v169, 0, 1, s[16:17]
	v_addc_co_u32_e32 v172, vcc, v168, v169, vcc
	ds_read_b128 v[168:171], v154 offset:1440
	s_waitcnt lgkmcnt(1)
	v_cmp_gt_f32_e64 s[16:17], v164, v159
	v_cmp_gt_f32_e32 vcc, v165, v159
	v_cmp_gt_f32_e64 s[98:99], v166, v159
	v_cndmask_b32_e64 v164, 0, 1, s[16:17]
	v_addc_co_u32_e32 v164, vcc, v172, v164, vcc
	v_cmp_gt_f32_e32 vcc, v167, v159
	v_cndmask_b32_e64 v165, 0, 1, s[98:99]
	s_nop 0
	v_addc_co_u32_e32 v164, vcc, v164, v165, vcc
	s_waitcnt lgkmcnt(0)
	v_cmp_gt_f32_e64 s[16:17], v168, v159
	v_cmp_gt_f32_e32 vcc, v169, v159
	s_nop 0
	v_cndmask_b32_e64 v165, 0, 1, s[16:17]
	v_addc_co_u32_e32 v168, vcc, v164, v165, vcc
	ds_read_b128 v[164:167], v154 offset:1456
	v_cmp_gt_f32_e64 s[16:17], v170, v159
	v_cmp_gt_f32_e32 vcc, v171, v159
	s_nop 0
	v_cndmask_b32_e64 v169, 0, 1, s[16:17]
	v_addc_co_u32_e32 v172, vcc, v168, v169, vcc
	ds_read_b128 v[168:171], v154 offset:1472
	s_waitcnt lgkmcnt(1)
	v_cmp_gt_f32_e64 s[16:17], v164, v159
	v_cmp_gt_f32_e32 vcc, v165, v159
	v_cmp_gt_f32_e64 s[98:99], v166, v159
	v_cndmask_b32_e64 v164, 0, 1, s[16:17]
	v_addc_co_u32_e32 v164, vcc, v172, v164, vcc
	v_cmp_gt_f32_e32 vcc, v167, v159
	v_cndmask_b32_e64 v165, 0, 1, s[98:99]
	s_nop 0
	v_addc_co_u32_e32 v164, vcc, v164, v165, vcc
	s_waitcnt lgkmcnt(0)
	v_cmp_gt_f32_e64 s[16:17], v168, v159
	v_cmp_gt_f32_e32 vcc, v169, v159
	s_nop 0
	v_cndmask_b32_e64 v165, 0, 1, s[16:17]
	v_addc_co_u32_e32 v164, vcc, v164, v165, vcc
	s_nop 0
	s_nop 0
	s_nop 0
	s_nop 0
	v_cmp_gt_u32_e32 vcc, 16, v164
	v_add_u32_e32 v164, 16, v164
	s_and_b64 vcc, s[4:5], vcc
	v_cndmask_b32_e32 v168, v151, v164, vcc
	ds_read_b128 v[164:167], v154 offset:1536
	v_lshlrev_b32_e32 v168, 2, v168
	ds_permute_b32 v159, v168, v159
	ds_permute_b32 v158, v168, v158
	ds_read_b128 v[168:171], v154 offset:1552
	s_waitcnt lgkmcnt(3)
	v_cmp_gt_f32_e32 vcc, v165, v157
	s_waitcnt lgkmcnt(2)
	v_cndmask_b32_e64 v159, v163, v159, s[46:47]
	v_cndmask_b32_e64 v165, 0, 1, vcc
	v_cmp_gt_f32_e32 vcc, v164, v157
	s_waitcnt lgkmcnt(1)
	v_cndmask_b32_e64 v158, v160, v158, s[46:47]
	v_addc_co_u32_e32 v164, vcc, 0, v165, vcc
	v_cmp_gt_f32_e64 s[16:17], v166, v157
	v_cmp_gt_f32_e32 vcc, v167, v157
	s_nop 0
	v_cndmask_b32_e64 v165, 0, 1, s[16:17]
	v_addc_co_u32_e32 v164, vcc, v164, v165, vcc
	s_waitcnt lgkmcnt(0)
	v_cmp_gt_f32_e64 s[16:17], v168, v157
	v_cmp_gt_f32_e32 vcc, v169, v157
	s_nop 0
	v_cndmask_b32_e64 v165, 0, 1, s[16:17]
	v_addc_co_u32_e32 v168, vcc, v164, v165, vcc
	ds_read_b128 v[164:167], v154 offset:1568
	v_cmp_gt_f32_e64 s[16:17], v170, v157
	v_cmp_gt_f32_e32 vcc, v171, v157
	s_nop 0
	v_cndmask_b32_e64 v169, 0, 1, s[16:17]
	v_addc_co_u32_e32 v172, vcc, v168, v169, vcc
	ds_read_b128 v[168:171], v154 offset:1584
	s_waitcnt lgkmcnt(1)
	v_cmp_gt_f32_e64 s[16:17], v164, v157
	v_cmp_gt_f32_e32 vcc, v165, v157
	v_cmp_gt_f32_e64 s[98:99], v166, v157
	v_cndmask_b32_e64 v164, 0, 1, s[16:17]
	v_addc_co_u32_e32 v164, vcc, v172, v164, vcc
	v_cmp_gt_f32_e32 vcc, v167, v157
	v_cndmask_b32_e64 v165, 0, 1, s[98:99]
	s_nop 0
	v_addc_co_u32_e32 v164, vcc, v164, v165, vcc
	s_waitcnt lgkmcnt(0)
	v_cmp_gt_f32_e64 s[16:17], v168, v157
	v_cmp_gt_f32_e32 vcc, v169, v157
	s_nop 0
	v_cndmask_b32_e64 v165, 0, 1, s[16:17]
	v_addc_co_u32_e32 v168, vcc, v164, v165, vcc
	ds_read_b128 v[164:167], v154 offset:1600
	v_cmp_gt_f32_e64 s[16:17], v170, v157
	v_cmp_gt_f32_e32 vcc, v171, v157
	s_nop 0
	v_cndmask_b32_e64 v169, 0, 1, s[16:17]
	v_addc_co_u32_e32 v172, vcc, v168, v169, vcc
	ds_read_b128 v[168:171], v154 offset:1616
	s_waitcnt lgkmcnt(1)
	v_cmp_gt_f32_e64 s[16:17], v164, v157
	v_cmp_gt_f32_e32 vcc, v165, v157
	v_cmp_gt_f32_e64 s[98:99], v166, v157
	v_cndmask_b32_e64 v164, 0, 1, s[16:17]
	v_addc_co_u32_e32 v164, vcc, v172, v164, vcc
	v_cmp_gt_f32_e32 vcc, v167, v157
	v_cndmask_b32_e64 v165, 0, 1, s[98:99]
	s_nop 0
	v_addc_co_u32_e32 v164, vcc, v164, v165, vcc
	s_waitcnt lgkmcnt(0)
	v_cmp_gt_f32_e64 s[16:17], v168, v157
	v_cmp_gt_f32_e32 vcc, v169, v157
	s_nop 0
	v_cndmask_b32_e64 v165, 0, 1, s[16:17]
	v_addc_co_u32_e32 v168, vcc, v164, v165, vcc
	ds_read_b128 v[164:167], v154 offset:1632
	v_cmp_gt_f32_e64 s[16:17], v170, v157
	v_cmp_gt_f32_e32 vcc, v171, v157
	s_nop 0
	v_cndmask_b32_e64 v169, 0, 1, s[16:17]
	v_addc_co_u32_e32 v172, vcc, v168, v169, vcc
	ds_read_b128 v[168:171], v154 offset:1648
	s_waitcnt lgkmcnt(1)
	v_cmp_gt_f32_e64 s[16:17], v164, v157
	v_cmp_gt_f32_e32 vcc, v165, v157
	v_cmp_gt_f32_e64 s[98:99], v166, v157
	v_cndmask_b32_e64 v164, 0, 1, s[16:17]
	v_addc_co_u32_e32 v164, vcc, v172, v164, vcc
	v_cmp_gt_f32_e32 vcc, v167, v157
	v_cndmask_b32_e64 v165, 0, 1, s[98:99]
	s_nop 0
	v_addc_co_u32_e32 v164, vcc, v164, v165, vcc
	s_waitcnt lgkmcnt(0)
	v_cmp_gt_f32_e64 s[16:17], v168, v157
	v_cmp_gt_f32_e32 vcc, v169, v157
	s_nop 0
	v_cndmask_b32_e64 v165, 0, 1, s[16:17]
	v_addc_co_u32_e32 v168, vcc, v164, v165, vcc
	ds_read_b128 v[164:167], v154 offset:1664
	v_cmp_gt_f32_e64 s[16:17], v170, v157
	v_cmp_gt_f32_e32 vcc, v171, v157
	s_nop 0
	v_cndmask_b32_e64 v169, 0, 1, s[16:17]
	v_addc_co_u32_e32 v172, vcc, v168, v169, vcc
	ds_read_b128 v[168:171], v154 offset:1680
	s_waitcnt lgkmcnt(1)
	v_cmp_gt_f32_e64 s[16:17], v164, v157
	v_cmp_gt_f32_e32 vcc, v165, v157
	v_cmp_gt_f32_e64 s[98:99], v166, v157
	v_cndmask_b32_e64 v164, 0, 1, s[16:17]
	v_addc_co_u32_e32 v164, vcc, v172, v164, vcc
	v_cmp_gt_f32_e32 vcc, v167, v157
	v_cndmask_b32_e64 v165, 0, 1, s[98:99]
	s_nop 0
	v_addc_co_u32_e32 v164, vcc, v164, v165, vcc
	s_waitcnt lgkmcnt(0)
	v_cmp_gt_f32_e64 s[16:17], v168, v157
	v_cmp_gt_f32_e32 vcc, v169, v157
	s_nop 0
	v_cndmask_b32_e64 v165, 0, 1, s[16:17]
	v_addc_co_u32_e32 v168, vcc, v164, v165, vcc
	ds_read_b128 v[164:167], v154 offset:1696
	v_cmp_gt_f32_e64 s[16:17], v170, v157
	v_cmp_gt_f32_e32 vcc, v171, v157
	s_nop 0
	v_cndmask_b32_e64 v169, 0, 1, s[16:17]
	v_addc_co_u32_e32 v172, vcc, v168, v169, vcc
	ds_read_b128 v[168:171], v154 offset:1712
	s_waitcnt lgkmcnt(1)
	v_cmp_gt_f32_e64 s[16:17], v164, v157
	v_cmp_gt_f32_e32 vcc, v165, v157
	v_cmp_gt_f32_e64 s[98:99], v166, v157
	v_cndmask_b32_e64 v164, 0, 1, s[16:17]
	v_addc_co_u32_e32 v164, vcc, v172, v164, vcc
	v_cmp_gt_f32_e32 vcc, v167, v157
	v_cndmask_b32_e64 v165, 0, 1, s[98:99]
	s_nop 0
	v_addc_co_u32_e32 v164, vcc, v164, v165, vcc
	s_waitcnt lgkmcnt(0)
	v_cmp_gt_f32_e64 s[16:17], v168, v157
	v_cmp_gt_f32_e32 vcc, v169, v157
	s_nop 0
	v_cndmask_b32_e64 v165, 0, 1, s[16:17]
	v_addc_co_u32_e32 v168, vcc, v164, v165, vcc
	ds_read_b128 v[164:167], v154 offset:1728
	v_cmp_gt_f32_e64 s[16:17], v170, v157
	v_cmp_gt_f32_e32 vcc, v171, v157
	s_nop 0
	v_cndmask_b32_e64 v169, 0, 1, s[16:17]
	v_addc_co_u32_e32 v172, vcc, v168, v169, vcc
	ds_read_b128 v[168:171], v154 offset:1792
	s_waitcnt lgkmcnt(1)
	v_cmp_gt_f32_e64 s[16:17], v164, v157
	v_cmp_gt_f32_e32 vcc, v165, v157
	s_nop 0
	v_cndmask_b32_e64 v164, 0, 1, s[16:17]
	v_addc_co_u32_e32 v164, vcc, v172, v164, vcc
	s_nop 0
	s_nop 0
	s_nop 0
	s_nop 0
	v_cmp_gt_u32_e32 vcc, 16, v164
	v_add_u32_e32 v164, 32, v164
	s_and_b64 vcc, s[4:5], vcc
	v_cndmask_b32_e32 v164, v152, v164, vcc
	v_lshlrev_b32_e32 v164, 2, v164
	ds_permute_b32 v157, v164, v157
	s_waitcnt lgkmcnt(1)
	v_cmp_gt_f32_e32 vcc, v169, v153
	ds_permute_b32 v155, v164, v155
	ds_read_b128 v[164:167], v154 offset:1808
	s_waitcnt lgkmcnt(2)
	v_cndmask_b32_e64 v157, v159, v157, s[48:49]
	v_cndmask_b32_e64 v159, 0, 1, vcc
	v_cmp_gt_f32_e32 vcc, v168, v153
	s_waitcnt lgkmcnt(1)
	v_cndmask_b32_e64 v155, v158, v155, s[48:49]
	v_addc_co_u32_e32 v159, vcc, 0, v159, vcc
	v_cmp_gt_f32_e32 vcc, v170, v153
	s_nop 1
	v_cndmask_b32_e64 v160, 0, 1, vcc
	v_cmp_gt_f32_e32 vcc, v171, v153
	ds_read_b128 v[168:171], v154 offset:1824
	s_nop 0
	v_addc_co_u32_e32 v159, vcc, v159, v160, vcc
	s_waitcnt lgkmcnt(1)
	v_cmp_gt_f32_e64 s[16:17], v164, v153
	v_cmp_gt_f32_e32 vcc, v165, v153
	s_nop 0
	v_cndmask_b32_e64 v160, 0, 1, s[16:17]
	v_addc_co_u32_e32 v159, vcc, v159, v160, vcc
	v_cmp_gt_f32_e32 vcc, v166, v153
	s_nop 1
	v_cndmask_b32_e64 v160, 0, 1, vcc
	v_cmp_gt_f32_e32 vcc, v167, v153
	ds_read_b128 v[164:167], v154 offset:1840
	s_nop 0
	v_addc_co_u32_e32 v159, vcc, v159, v160, vcc
	s_waitcnt lgkmcnt(1)
	v_cmp_gt_f32_e64 s[16:17], v168, v153
	v_cmp_gt_f32_e32 vcc, v169, v153
	s_nop 0
	v_cndmask_b32_e64 v160, 0, 1, s[16:17]
	v_addc_co_u32_e32 v159, vcc, v159, v160, vcc
	v_cmp_gt_f32_e32 vcc, v170, v153
	s_nop 1
	v_cndmask_b32_e64 v160, 0, 1, vcc
	v_cmp_gt_f32_e32 vcc, v171, v153
	ds_read_b128 v[168:171], v154 offset:1856
	s_nop 0
	v_addc_co_u32_e32 v159, vcc, v159, v160, vcc
	s_waitcnt lgkmcnt(1)
	v_cmp_gt_f32_e64 s[16:17], v164, v153
	v_cmp_gt_f32_e32 vcc, v165, v153
	s_nop 0
	v_cndmask_b32_e64 v160, 0, 1, s[16:17]
	v_addc_co_u32_e32 v159, vcc, v159, v160, vcc
	v_cmp_gt_f32_e32 vcc, v166, v153
	s_nop 1
	v_cndmask_b32_e64 v160, 0, 1, vcc
	v_cmp_gt_f32_e32 vcc, v167, v153
	ds_read_b128 v[164:167], v154 offset:1872
	s_nop 0
	v_addc_co_u32_e32 v159, vcc, v159, v160, vcc
	s_waitcnt lgkmcnt(1)
	v_cmp_gt_f32_e64 s[16:17], v168, v153
	v_cmp_gt_f32_e32 vcc, v169, v153
	s_nop 0
	v_cndmask_b32_e64 v160, 0, 1, s[16:17]
	v_addc_co_u32_e32 v159, vcc, v159, v160, vcc
	v_cmp_gt_f32_e32 vcc, v170, v153
	s_nop 1
	v_cndmask_b32_e64 v160, 0, 1, vcc
	v_cmp_gt_f32_e32 vcc, v171, v153
	ds_read_b128 v[168:171], v154 offset:1888
	s_nop 0
	v_addc_co_u32_e32 v159, vcc, v159, v160, vcc
	s_waitcnt lgkmcnt(1)
	v_cmp_gt_f32_e64 s[16:17], v164, v153
	v_cmp_gt_f32_e32 vcc, v165, v153
	s_nop 0
	v_cndmask_b32_e64 v160, 0, 1, s[16:17]
	v_addc_co_u32_e32 v159, vcc, v159, v160, vcc
	v_cmp_gt_f32_e32 vcc, v166, v153
	s_nop 1
	v_cndmask_b32_e64 v160, 0, 1, vcc
	v_cmp_gt_f32_e32 vcc, v167, v153
	ds_read_b128 v[164:167], v154 offset:1904
	s_nop 0
	v_addc_co_u32_e32 v159, vcc, v159, v160, vcc
	s_waitcnt lgkmcnt(1)
	v_cmp_gt_f32_e64 s[16:17], v168, v153
	v_cmp_gt_f32_e32 vcc, v169, v153
	s_nop 0
	v_cndmask_b32_e64 v160, 0, 1, s[16:17]
	v_addc_co_u32_e32 v159, vcc, v159, v160, vcc
	v_cmp_gt_f32_e32 vcc, v170, v153
	s_nop 1
	v_cndmask_b32_e64 v160, 0, 1, vcc
	v_cmp_gt_f32_e32 vcc, v171, v153
	ds_read_b128 v[168:171], v154 offset:1920
	s_nop 0
	v_addc_co_u32_e32 v159, vcc, v159, v160, vcc
	s_waitcnt lgkmcnt(1)
	v_cmp_gt_f32_e64 s[16:17], v164, v153
	v_cmp_gt_f32_e32 vcc, v165, v153
	s_nop 0
	v_cndmask_b32_e64 v160, 0, 1, s[16:17]
	v_addc_co_u32_e32 v159, vcc, v159, v160, vcc
	v_cmp_gt_f32_e32 vcc, v166, v153
	s_nop 1
	v_cndmask_b32_e64 v160, 0, 1, vcc
	v_cmp_gt_f32_e32 vcc, v167, v153
	ds_read_b128 v[164:167], v154 offset:1936
	s_nop 0
	v_addc_co_u32_e32 v159, vcc, v159, v160, vcc
	s_waitcnt lgkmcnt(1)
	v_cmp_gt_f32_e64 s[16:17], v168, v153
	v_cmp_gt_f32_e32 vcc, v169, v153
	s_nop 0
	v_cndmask_b32_e64 v160, 0, 1, s[16:17]
	v_addc_co_u32_e32 v159, vcc, v159, v160, vcc
	v_cmp_gt_f32_e32 vcc, v170, v153
	s_nop 1
	v_cndmask_b32_e64 v160, 0, 1, vcc
	v_cmp_gt_f32_e32 vcc, v171, v153
	ds_read_b128 v[168:171], v154 offset:1952
	s_nop 0
	v_addc_co_u32_e32 v159, vcc, v159, v160, vcc
	s_waitcnt lgkmcnt(1)
	v_cmp_gt_f32_e64 s[16:17], v164, v153
	v_cmp_gt_f32_e32 vcc, v165, v153
	s_nop 0
	v_cndmask_b32_e64 v160, 0, 1, s[16:17]
	v_addc_co_u32_e32 v159, vcc, v159, v160, vcc
	v_cmp_gt_f32_e32 vcc, v166, v153
	s_nop 1
	v_cndmask_b32_e64 v160, 0, 1, vcc
	v_cmp_gt_f32_e32 vcc, v167, v153
	ds_read_b128 v[164:167], v154 offset:1968
	s_nop 0
	v_addc_co_u32_e32 v159, vcc, v159, v160, vcc
	s_waitcnt lgkmcnt(1)
	v_cmp_gt_f32_e64 s[16:17], v168, v153
	v_cmp_gt_f32_e32 vcc, v169, v153
	s_nop 0
	v_cndmask_b32_e64 v160, 0, 1, s[16:17]
	v_addc_co_u32_e32 v159, vcc, v159, v160, vcc
	v_cmp_gt_f32_e32 vcc, v170, v153
	s_nop 1
	v_cndmask_b32_e64 v160, 0, 1, vcc
	v_cmp_gt_f32_e32 vcc, v171, v153
	ds_read_b128 v[168:171], v154 offset:1984
	s_nop 0
	v_addc_co_u32_e32 v159, vcc, v159, v160, vcc
	s_waitcnt lgkmcnt(1)
	v_cmp_gt_f32_e32 vcc, v164, v153
	v_max_f32_e32 v160, v162, v162
	s_nop 0
	v_cndmask_b32_e64 v154, 0, 1, vcc
	v_cmp_gt_f32_e32 vcc, v165, v153
	s_nop 1
	v_addc_co_u32_e32 v154, vcc, v159, v154, vcc
	v_cmp_gt_f32_e64 s[16:17], v166, v153
	v_cmp_gt_f32_e32 vcc, v167, v153
	s_nop 0
	v_cndmask_b32_e64 v159, 0, 1, s[16:17]
	v_addc_co_u32_e32 v154, vcc, v154, v159, vcc
	s_waitcnt lgkmcnt(0)
	v_cmp_gt_f32_e64 s[16:17], v168, v153
	v_cmp_gt_f32_e32 vcc, v169, v153
	s_nop 0
	v_cndmask_b32_e64 v159, 0, 1, s[16:17]
	v_addc_co_u32_e32 v154, vcc, v154, v159, vcc
	s_nop 0
	s_nop 0
	s_nop 0
	s_nop 0
	v_mov_b32_e32 v159, v201
	v_cmp_gt_u32_e32 vcc, 16, v154
	v_add_u32_e32 v154, 48, v154
	v_mov_b32_dpp v159, v162 row_ror:1 row_mask:0xf bank_mask:0xf
	v_max_f32_e32 v159, v159, v159
	v_max_f32_e32 v159, v160, v159
	s_nop 0
	s_and_b64 vcc, s[4:5], vcc
	v_cndmask_b32_e32 v154, v140, v154, vcc
	v_max_f32_dpp v159, v159, v159 row_ror:2 row_mask:0xf bank_mask:0xf
	s_nop 0
	s_nop 0
	s_nop 0
	v_lshlrev_b32_e32 v154, 2, v154
	ds_permute_b32 v153, v154, v153
	v_max_f32_dpp v159, v159, v159 row_ror:4 row_mask:0xf bank_mask:0xf
	s_nop 0
	s_nop 0
	s_nop 0
	ds_permute_b32 v154, v154, v156
	s_waitcnt lgkmcnt(1)
	v_cndmask_b32_e64 v153, v157, v153, s[50:51]
	v_max_f32_dpp v159, v159, v159 row_ror:8 row_mask:0xf bank_mask:0xf
	s_nop 0
	s_nop 0
	v_sub_f32_e32 v159, v162, v159
	v_mul_f32_e32 v159, 0x3fb8aa3b, v159
	v_exp_f32_e32 v159, v159
	s_waitcnt lgkmcnt(0)
	v_cndmask_b32_e64 v158, v155, v154, s[50:51]
	v_add_f32_dpp v156, v159, v159 row_ror:1 row_mask:0xf bank_mask:0xf bound_ctrl:1
	s_nop 1
	v_add_f32_dpp v156, v156, v156 row_ror:2 row_mask:0xf bank_mask:0xf bound_ctrl:1
	s_nop 1
	v_add_f32_dpp v156, v156, v156 row_ror:4 row_mask:0xf bank_mask:0xf bound_ctrl:1
	s_nop 1
	v_add_f32_dpp v156, v156, v156 row_ror:8 row_mask:0xf bank_mask:0xf bound_ctrl:1
	v_div_scale_f32 v160, s[80:81], v156, v156, v159
	v_rcp_f32_e32 v162, v160
	s_mov_b32 s80, 0x31200000
	v_fma_f32 v154, -v160, v162, 1.0
	v_fmac_f32_e32 v162, v154, v162
	v_div_scale_f32 v154, vcc, v159, v156, v159
	v_mul_f32_e32 v155, v154, v162
	v_fma_f32 v157, -v160, v155, v154
	v_fmac_f32_e32 v155, v157, v162
	v_fma_f32 v154, -v160, v155, v154
	v_mov_b32_e32 v157, v201
	v_div_fmas_f32 v154, v154, v162, v155
	v_div_fixup_f32 v156, v154, v156, v159
	v_mov_b32_dpp v157, v153 row_ror:1 row_mask:0xf bank_mask:0xf
	v_max_f32_e32 v159, v153, v153
	v_max_f32_e32 v157, v157, v157
	v_max_f32_e32 v157, v159, v157
	s_nop 0
	v_lshl_add_u64 v[154:155], s[92:93], 0, v[132:133]
	v_add_co_u32_e32 v154, vcc, s80, v154
	v_max_f32_dpp v157, v157, v157 row_ror:2 row_mask:0xf bank_mask:0xf
	s_nop 0
	s_nop 0
	s_nop 0
	v_addc_co_u32_e32 v155, vcc, 0, v155, vcc
	s_nop 0
	v_max_f32_dpp v157, v157, v157 row_ror:4 row_mask:0xf bank_mask:0xf
	s_nop 0
	s_nop 0
	s_nop 0
	global_store_dword v[154:155], v156, off
	s_nop 0
	v_max_f32_dpp v157, v157, v157 row_ror:8 row_mask:0xf bank_mask:0xf
	s_nop 0
	s_nop 0
	v_sub_f32_e32 v153, v153, v157
	v_mul_f32_e32 v153, 0x3fb8aa3b, v153
	v_exp_f32_e32 v153, v153
	s_nop 1
	v_add_f32_dpp v156, v153, v153 row_ror:1 row_mask:0xf bank_mask:0xf bound_ctrl:1
	s_nop 1
	v_add_f32_dpp v156, v156, v156 row_ror:2 row_mask:0xf bank_mask:0xf bound_ctrl:1
	s_nop 1
	v_add_f32_dpp v156, v156, v156 row_ror:4 row_mask:0xf bank_mask:0xf bound_ctrl:1
	s_nop 1
	v_add_f32_dpp v159, v156, v156 row_ror:8 row_mask:0xf bank_mask:0xf bound_ctrl:1
	v_div_scale_f32 v160, s[80:81], v159, v159, v153
	v_rcp_f32_e32 v162, v160
	v_lshl_add_u64 v[156:157], s[92:93], 0, v[134:135]
	global_store_dword v[156:157], v161, off
	v_fma_f32 v156, -v160, v162, 1.0
	v_fmac_f32_e32 v162, v156, v162
	v_div_scale_f32 v156, vcc, v153, v159, v153
	v_mul_f32_e32 v157, v156, v162
	v_fma_f32 v161, -v160, v157, v156
	v_fmac_f32_e32 v157, v161, v162
	v_fma_f32 v156, -v160, v157, v156
	v_div_fmas_f32 v156, v156, v162, v157
	v_div_fixup_f32 v153, v156, v159, v153
	global_store_dword v[154:155], v153, off offset:256
	v_lshlrev_b32_e32 v153, 7, v158
	v_lshl_add_u64 v[154:155], s[92:93], 0, v[136:137]
	s_and_b64 vcc, exec, s[52:53]
	global_store_dword v[154:155], v153, off
	s_cbranch_vccnz .LBB0_1847
	v_readlane_b32 s10, v254, 10
	v_readlane_b32 s11, v254, 11
	s_andn2_b64 vcc, exec, s[10:11]
	s_cbranch_vccnz .LBB0_1871
	global_load_dwordx4 v[164:167], v[112:113], off
	global_load_dwordx4 v[168:171], v[112:113], off offset:16
	global_load_dwordx4 v[172:175], v[112:113], off offset:32
	global_load_dwordx4 v[176:179], v[112:113], off offset:48
	global_load_dwordx4 v[180:183], v[114:115], off
	global_load_dwordx4 v[184:187], v[116:117], off
	global_load_dwordx4 v[188:191], v[118:119], off
	global_load_dwordx4 v[192:195], v[120:121], off
	s_waitcnt vmcnt(0)
	v_pk_mul_f32 v[46:47], v[46:47], v[166:167]
	v_pk_mul_f32 v[44:45], v[44:45], v[164:165]
	v_pk_mul_f32 v[42:43], v[42:43], v[170:171]
	v_pk_mul_f32 v[40:41], v[40:41], v[168:169]
	v_pk_mul_f32 v[38:39], v[38:39], v[174:175]
	v_pk_mul_f32 v[36:37], v[36:37], v[172:173]
	v_pk_mul_f32 v[34:35], v[34:35], v[178:179]
	v_pk_mul_f32 v[32:33], v[32:33], v[176:177]
	v_pk_mul_f32 v[50:51], v[50:51], v[182:183]
	v_pk_mul_f32 v[48:49], v[48:49], v[180:181]
	v_pk_mul_f32 v[62:63], v[62:63], v[186:187]
	v_pk_mul_f32 v[60:61], v[60:61], v[184:185]
	v_pk_mul_f32 v[58:59], v[58:59], v[190:191]
	v_pk_mul_f32 v[56:57], v[56:57], v[188:189]
	v_pk_mul_f32 v[54:55], v[54:55], v[194:195]
	v_pk_mul_f32 v[52:53], v[52:53], v[192:193]

.LBB0_1875:
	v_sub_u32_e32 v139, 0x7f, v139
	v_sub_u32_e32 v143, 0x7f, v143
	v_sub_u32_e32 v144, 0x7f, v144
	v_sub_u32_e32 v145, 0x7f, v145
	v_readlane_b32 s78, v251, 36
	v_readlane_b32 s66, v255, 37
	v_readlane_b32 s96, v255, 39
	v_readlane_b32 s68, v251, 54
	v_readlane_b32 s69, v251, 55
	v_readlane_b32 s62, v251, 56
	v_readlane_b32 s63, v251, 57
	v_readlane_b32 s79, v251, 37
	s_mov_b32 s80, s8
	v_readlane_b32 s67, v255, 38
	v_readlane_b32 s97, v255, 40
	s_mov_b64 s[74:75], s[12:13]
	s_mov_b64 s[52:53], s[14:15]
	v_readlane_b32 s38, v255, 45
	v_readlane_b32 s39, v255, 46
